# attention loop with fewer instructions per tile: LDS waits once per two fragments (K 8-deep, V 6-deep prefetch), DMA block without the last-tile barrier guard and with one running pointer (V offsets c
# speedup vs baseline: 1.0252x; 1.0061x over previous
; __device__ __forceinline__ void attn_dma_body(const bf16_t* __restrict__ Qb, int ldq, int tpos0, const float* __restrict__ rope, const float* __restrict__ qgain, ...
;     ...
;   ATT_DMA(0, 0); ATT_DMA(1, 1);
; #pragma unroll
;   for (int d0 = 0; d0 < 8; ++d0) qr[d0] = ld8(Qw + d0 * 16);
;   if (tpos0 >= 0) {
;     float ss = 0.f;
; #pragma unroll
;     for (int d0 = 0; d0 < 8; ++d0)
; #pragma unroll
;       for (int i = 0; i < 8; ++i) { const float x = bf2f((unsigned)(unsigned short)qr[d0][i]); ss += x * x; }
;     { auto rr = __builtin_amdgcn_permlane32_swap(__float_as_uint(ss), __float_as_uint(ss), false, false); ss = __uint_as_float(rr[0]) + __uint_as_float(rr[1]); }
;     const float rinv = 1.0f / sqrtf(ss * (1.0f / 128.0f) + RMS_EPS);
;     const int t = tpos0 + wid * QBLK + r32;
; #pragma unroll
;     for (int ax = 0; ax < 2; ++ax) { const int pos = ax ? (t & 63) : (t >> 6);
; #pragma unroll
;       for (int q = 0; q < 2; ++q) { const int dl = 4 * ax + q, dh = dl + 2, p0 = q * 16 + 8 * hi;
;         const float* cp_ = rope + pos * 32 + p0; const float* gl = qgain + dl * 16 + 8 * hi; const float* gh = qgain + dh * 16 + 8 * hi;
;         float cs[8], sn[8], lo[8], hv[8];
; #pragma unroll
;         for (int i = 0; i < 8; ++i) { cs[i] = cp_[i]; sn[i] = cp_[4096 + i];
;           lo[i] = bf2f((unsigned)(unsigned short)qr[dl][i]) * rinv * gl[i]; hv[i] = bf2f((unsigned)(unsigned short)qr[dh][i]) * rinv * gh[i]; }
;         u32x4 wl, wh;
; #pragma unroll
;         for (int i = 0; i < 4; ++i) { const float l0 = lo[2 * i] * cs[2 * i] - hv[2 * i] * sn[2 * i], l1 = lo[2 * i + 1] * cs[2 * i + 1] - hv[2 * i + 1] * sn[2 * i + 1];
;           const float h0 = hv[2 * i] * cs[2 * i] + lo[2 * i] * sn[2 * i], h1 = hv[2 * i + 1] * cs[2 * i + 1] + lo[2 * i + 1] * sn[2 * i + 1];
;           wl[i] = pk2(l0, l1); wh[i] = pk2(h0, h1); }
;         qr[dl] = *reinterpret_cast<bf16x8*>(&wl); qr[dh] = *reinterpret_cast<bf16x8*>(&wh); } } }
; #pragma unroll
;   for (int d0 = 0; d0 < 8; ++d0) asm volatile("" : "+v"(qr[d0]));
;   ATT_WAIT_BAR();
;   if (2 < NT) ATT_DMA(2, 2);
;   const int vb0 = (int)(uintptr_t)lds + 16384 + v_rd_base(lane);
;   f32x16 pA0, pA1, pB0, pB1; float mnA, mnB, alA, alB; bf16x8 pa0, pa1, pa2, pa3;
;   qkt(pA0, pA1, (const bf16_t*)lds, qr, r32, hi); partialSM(pA0, pA1, m_reg, mnA, alA);
;   const bool lead = __builtin_amdgcn_readfirstlane(wid) < 4;
.LBB0_408:
	v_and_b32_e32 v167, 63, v147
	v_and_b32_e32 v246, 15, v167
	v_lshrrev_b32_e32 v247, 4, v167
	v_lshlrev_b32_e32 v248, 13, v179
	v_add_u32_e32 v248, 0x10000, v248
	v_lshl_add_u32 v249, v177, 8, v248
	v_lshl_add_u32 v249, v178, 4, v249
	ds_write_b128 v249, v[102:105] offset:0
	ds_write_b128 v249, v[110:113] offset:32
	ds_write_b128 v249, v[98:101] offset:64
	ds_write_b128 v249, v[106:109] offset:96
	ds_write_b128 v249, v[118:121] offset:128
	ds_write_b128 v249, v[126:129] offset:160
	ds_write_b128 v249, v[114:117] offset:192
	ds_write_b128 v249, v[122:125] offset:224
	v_lshl_add_u32 v251, v246, 8, v248
	v_lshl_add_u32 v251, v247, 4, v251
	s_waitcnt lgkmcnt(0)
	ds_read_b128 v[98:101], v251 offset:0
	ds_read_b128 v[102:105], v251 offset:64
	ds_read_b128 v[106:109], v251 offset:128
	ds_read_b128 v[110:113], v251 offset:192
	ds_read_b128 v[114:117], v251 offset:4096
	ds_read_b128 v[118:121], v251 offset:4160
	ds_read_b128 v[122:125], v251 offset:4224
	ds_read_b128 v[126:129], v251 offset:4288
	v_lshlrev_b32_e32 v252, 4, v246
	v_lshlrev_b32_e32 v253, 4, v247
	v_lshlrev_b32_e32 v254, 8, v246
	v_or_b32_e32 v255, 0, v253
	v_xor_b32_e32 v255, v255, v252
	v_or_b32_e32 v183, v255, v254
	v_or_b32_e32 v255, 64, v253
	v_xor_b32_e32 v255, v255, v252
	v_or_b32_e32 v184, v255, v254
	v_or_b32_e32 v255, 128, v253
	v_xor_b32_e32 v255, v255, v252
	v_or_b32_e32 v185, v255, v254
	v_or_b32_e32 v255, 192, v253
	v_xor_b32_e32 v255, v255, v252
	v_or_b32_e32 v186, v255, v254
	v_lshrrev_b32_e32 v252, 1, v247
	v_lshlrev_b32_e32 v252, 11, v252
	v_and_b32_e32 v253, 1, v247
	v_lshl_add_u32 v252, v253, 8, v252
	v_lshrrev_b32_e32 v254, 2, v246
	v_lshl_add_u32 v252, v254, 6, v252
	v_and_b32_e32 v254, 3, v246
	v_lshl_add_u32 v252, v254, 3, v252
	v_lshl_add_u32 v191, v253, 5, v252
	v_xor_b32_e32 v253, 1, v253
	v_lshl_add_u32 v192, v253, 5, v252
	v_add_u32_e32 v191, 0x4000, v191
	v_add_u32_e32 v192, 0x4000, v192
	v_readfirstlane_b32 s42, v179
	v_mov_b32_e32 v170, v162
	v_mov_b32_e32 v172, v32
	v_mov_b32_e32 v171, v30
	v_mov_b32_e32 v173, v34
	v_add_u32_e32 v171, 0x1100000, v171
	v_add_u32_e32 v173, 0x1100000, v173
	v_mov_b32_e32 v2, 0
	v_mov_b32_e32 v3, 0
	v_mov_b32_e32 v4, 0
	v_mov_b32_e32 v5, 0
	v_mov_b32_e32 v6, 0
	v_mov_b32_e32 v7, 0
	v_mov_b32_e32 v8, 0
	v_mov_b32_e32 v9, 0
	v_mov_b32_e32 v10, 0
	v_mov_b32_e32 v11, 0
	v_mov_b32_e32 v12, 0
	v_mov_b32_e32 v13, 0
	v_mov_b32_e32 v14, 0
	v_mov_b32_e32 v15, 0
	v_mov_b32_e32 v16, 0
	v_mov_b32_e32 v17, 0
	v_mov_b32_e32 v18, 0
	v_mov_b32_e32 v19, 0
	v_mov_b32_e32 v20, 0
	v_mov_b32_e32 v21, 0
	v_mov_b32_e32 v22, 0
	v_mov_b32_e32 v23, 0
	v_mov_b32_e32 v24, 0
	v_mov_b32_e32 v25, 0
	v_mov_b32_e32 v26, 0
	v_mov_b32_e32 v27, 0
	v_mov_b32_e32 v28, 0
	v_mov_b32_e32 v29, 0
	v_mov_b32_e32 v30, 0
	v_mov_b32_e32 v31, 0
	v_mov_b32_e32 v32, 0
	v_mov_b32_e32 v33, 0
	v_mov_b32_e32 v34, 0
	v_mov_b32_e32 v35, 0
	v_mov_b32_e32 v36, 0
	v_mov_b32_e32 v37, 0
	v_mov_b32_e32 v38, 0
	v_mov_b32_e32 v39, 0
	v_mov_b32_e32 v40, 0
	v_mov_b32_e32 v41, 0
	v_mov_b32_e32 v42, 0
	v_mov_b32_e32 v43, 0
	v_mov_b32_e32 v44, 0
	v_mov_b32_e32 v45, 0
	v_mov_b32_e32 v46, 0
	v_mov_b32_e32 v47, 0
	v_mov_b32_e32 v48, 0
	v_mov_b32_e32 v49, 0
	v_mov_b32_e32 v50, 0
	v_mov_b32_e32 v51, 0
	v_mov_b32_e32 v52, 0
	v_mov_b32_e32 v53, 0
	v_mov_b32_e32 v54, 0
	v_mov_b32_e32 v55, 0
	v_mov_b32_e32 v56, 0
	v_mov_b32_e32 v57, 0
	v_mov_b32_e32 v58, 0
	v_mov_b32_e32 v59, 0
	v_mov_b32_e32 v60, 0
	v_mov_b32_e32 v61, 0
	v_mov_b32_e32 v62, 0
	v_mov_b32_e32 v63, 0
	v_mov_b32_e32 v64, 0
	v_mov_b32_e32 v65, 0
	v_mov_b32_e32 v182, 0
	v_mov_b32_e32 v195, 0
	v_mov_b32_e32 v246, 0
	v_mov_b32_e32 v247, 0
	v_mov_b32_e32 v248, 0
	v_mov_b32_e32 v249, 0
	v_mov_b32_e32 v252, 0
	v_mov_b32_e32 v253, 0
	v_mov_b32_e32 v254, 0
	v_mov_b32_e32 v255, 0
	v_mov_b32_e32 v194, 0x3f803f80
	v_mov_b32_e32 v195, 0x3f803f80
	v_mov_b32_e32 v196, 0x3f803f80
	v_mov_b32_e32 v197, 0x3f803f80
	s_cmp_lt_u32 s42, 4
	s_cbranch_scc1 .Lf16_noprio
	s_setprio 1
.Lf16_noprio:
	s_waitcnt vmcnt(0) lgkmcnt(0)
	s_barrier
	s_add_u32 s2, s38, 0x8000
	s_addc_u32 s3, s39, 0
	s_add_u32 s4, s40, 0x8000
	s_addc_u32 s5, s41, 0
	s_add_i32 s6, s96, 0x10000
	s_add_i32 m0, s96, 0x10000
	s_nop 0
	global_load_lds_dwordx4 v170, s[2:3]
	s_add_i32 m0, s96, 0x12000
	s_nop 0
	global_load_lds_dwordx4 v172, s[2:3]
	s_add_i32 m0, s96, 0x14000
	s_nop 0
	global_load_lds_dwordx4 v171, s[2:3]
	s_add_i32 m0, s96, 0x16000
	s_nop 0
	global_load_lds_dwordx4 v173, s[2:3]
	s_add_u32 s2, s2, 0x4000
	s_addc_u32 s3, s3, 0
	v_add_u32_e32 v187, 0x10000, v183
	v_add_u32_e32 v188, 0x10000, v184
	v_add_u32_e32 v189, 0x10000, v185
	v_add_u32_e32 v190, 0x10000, v186
	v_add_u32_e32 v180, 0x10000, v191
	v_add_u32_e32 v181, 0x10000, v192
	s_mov_b32 s36, 0
	ds_read_b128 v[146:149], v183 offset:0
	ds_read_b128 v[150:153], v183 offset:4096
	ds_read_b128 v[154:157], v183 offset:8192
	ds_read_b128 v[158:161], v183 offset:12288
	ds_read_b128 v[198:201], v184 offset:0
	ds_read_b128 v[202:205], v184 offset:4096
	ds_read_b128 v[206:209], v184 offset:8192
	ds_read_b128 v[210:213], v184 offset:12288
	s_waitcnt lgkmcnt(6)
	v_mfma_f32_16x16x32_bf16 v[66:69], v[146:149], v[98:101], 0
	v_mfma_f32_16x16x32_bf16 v[70:73], v[146:149], v[114:117], 0
	v_mfma_f32_16x16x32_bf16 v[74:77], v[150:153], v[98:101], 0
	v_mfma_f32_16x16x32_bf16 v[78:81], v[150:153], v[114:117], 0
	ds_read_b128 v[146:149], v185 offset:0
	ds_read_b128 v[150:153], v185 offset:4096
	s_waitcnt lgkmcnt(6)
	v_mfma_f32_16x16x32_bf16 v[82:85], v[154:157], v[98:101], 0
	v_mfma_f32_16x16x32_bf16 v[86:89], v[154:157], v[114:117], 0
	v_mfma_f32_16x16x32_bf16 v[90:93], v[158:161], v[98:101], 0
	v_mfma_f32_16x16x32_bf16 v[94:97], v[158:161], v[114:117], 0
	ds_read_b128 v[154:157], v185 offset:8192
	ds_read_b128 v[158:161], v185 offset:12288
	s_waitcnt lgkmcnt(6)
; #define SBAR() __builtin_amdgcn_sched_barrier(0)
; #define RESC(a) do { if (__any((a) < 1.f)) { if (hi == 0) al_l[r32] = (a); asm volatile("s_waitcnt lgkmcnt(0)" ::: "memory"); \
;     for (int d = 0; d < 4; ++d) for (int r = 0; r < 16; ++r) o[d][r] *= al_l[crow(r, hi)]; } } while (0)
; #define RESC(a) do { if (__any((a) < 1.f)) { if (hi == 0) al_l[r32] = (a); asm volatile("s_waitcnt lgkmcnt(0)" ::: "memory"); \
;     for (int d = 0; d < 4; ++d) for (int r = 0; r < 16; ++r) o[d][r] *= al_l[crow(r, hi)]; } } while (0)
; __device__ __forceinline__ void qkt(f32x16& p0, f32x16& p1, const bf16_t* Ks, const bf16x8* qr, int r32, int hi) {
;   p0 = f32x16{}; p1 = f32x16{};
;   for (int d0 = 0; d0 < 8; ++d0) { int cb = (d0 * 16 + hi * 8) * 2;
;     bf16x8 b0 = *reinterpret_cast<const bf16x8*>((const char*)Ks + KSWZ(r32, cb));
;     bf16x8 b1 = *reinterpret_cast<const bf16x8*>((const char*)Ks + KSWZ(32 + r32, cb));
;     p0 = __builtin_amdgcn_mfma_f32_32x32x16_bf16(b0, qr[d0], p0, 0, 0, 0);
;     p1 = __builtin_amdgcn_mfma_f32_32x32x16_bf16(b1, qr[d0], p1, 0, 0, 0); }
; }
; __device__ __forceinline__ void attn_dma_body(const bf16_t* __restrict__ Qb, int ldq, int tpos0, const float* __restrict__ rope, const float* __restrict__ qgain, ...
;     ...
;   qkt(pA0, pA1, (const bf16_t*)lds, qr, r32, hi); partialSM(pA0, pA1, m_reg, mnA, alA);
;   const bool lead = __builtin_amdgcn_readfirstlane(wid) < 4;
;     ...
;   for (int j = 1; j + 1 < NT; j += 2) {
;     { SBAR(); qkt(pB0, pB1, (const bf16_t*)(lds + (j & 3) * SHM_SLOT), qr, r32, hi);
;       finishSM(pA0, pA1, alA, l_reg, pa0, pa1, pa2, pa3); s16x4 va[8]; pv_rd<0>(va, vb0 + ((j - 1) & 3) * (int)SHM_SLOT); SBAR();
;       if (!lead) ATT_SYNC(j + 2);
;       pv_d0_pre(o, vb0 + ((j - 1) & 3) * (int)SHM_SLOT, va, pa0, pa1, pa2, pa3); partialSM(pB0, pB1, m_reg, mnB, alB);
;       if (lead) ATT_SYNC(j + 2);
;       RESC(alB); }
;     { SBAR(); qkt(pA0, pA1, (const bf16_t*)(lds + ((j + 1) & 3) * SHM_SLOT), qr, r32, hi);
;       finishSM(pB0, pB1, alB, l_reg, pa0, pa1, pa2, pa3); s16x4 va[8]; pv_rd<0>(va, vb0 + (j & 3) * (int)SHM_SLOT); SBAR();
;       if (!lead) ATT_SYNC(j + 3);
;       pv_d0_pre(o, vb0 + (j & 3) * (int)SHM_SLOT, va, pa0, pa1, pa2, pa3); partialSM(pA0, pA1, m_reg, mnA, alA);
;       if (lead) ATT_SYNC(j + 3);
;       RESC(alA); }
;   }
	v_mfma_f32_16x16x32_bf16 v[66:69], v[198:201], v[102:105], v[66:69]
	v_mfma_f32_16x16x32_bf16 v[70:73], v[198:201], v[118:121], v[70:73]
	v_mfma_f32_16x16x32_bf16 v[74:77], v[202:205], v[102:105], v[74:77]
	v_mfma_f32_16x16x32_bf16 v[78:81], v[202:205], v[118:121], v[78:81]
	ds_read_b128 v[198:201], v186 offset:0
	ds_read_b128 v[202:205], v186 offset:4096
	s_waitcnt lgkmcnt(6)
	v_mfma_f32_16x16x32_bf16 v[82:85], v[206:209], v[102:105], v[82:85]
	v_mfma_f32_16x16x32_bf16 v[86:89], v[206:209], v[118:121], v[86:89]
	v_mfma_f32_16x16x32_bf16 v[90:93], v[210:213], v[102:105], v[90:93]
	v_mfma_f32_16x16x32_bf16 v[94:97], v[210:213], v[118:121], v[94:97]
	ds_read_b128 v[206:209], v186 offset:8192
	ds_read_b128 v[210:213], v186 offset:12288
	s_waitcnt lgkmcnt(6)
	v_mfma_f32_16x16x32_bf16 v[66:69], v[146:149], v[106:109], v[66:69]
	v_mfma_f32_16x16x32_bf16 v[70:73], v[146:149], v[122:125], v[70:73]
	v_mfma_f32_16x16x32_bf16 v[74:77], v[150:153], v[106:109], v[74:77]
	v_mfma_f32_16x16x32_bf16 v[78:81], v[150:153], v[122:125], v[78:81]
	s_waitcnt lgkmcnt(4)
	v_mfma_f32_16x16x32_bf16 v[82:85], v[154:157], v[106:109], v[82:85]
	v_mfma_f32_16x16x32_bf16 v[86:89], v[154:157], v[122:125], v[86:89]
	v_mfma_f32_16x16x32_bf16 v[90:93], v[158:161], v[106:109], v[90:93]
	v_mfma_f32_16x16x32_bf16 v[94:97], v[158:161], v[122:125], v[94:97]
	s_waitcnt lgkmcnt(2)
	v_mfma_f32_16x16x32_bf16 v[66:69], v[198:201], v[110:113], v[66:69]
	v_mfma_f32_16x16x32_bf16 v[70:73], v[198:201], v[126:129], v[70:73]
	v_mfma_f32_16x16x32_bf16 v[74:77], v[202:205], v[110:113], v[74:77]
	v_mfma_f32_16x16x32_bf16 v[78:81], v[202:205], v[126:129], v[78:81]
	s_waitcnt lgkmcnt(0)
	v_mfma_f32_16x16x32_bf16 v[82:85], v[206:209], v[110:113], v[82:85]
	v_mfma_f32_16x16x32_bf16 v[86:89], v[206:209], v[126:129], v[86:89]
	v_mfma_f32_16x16x32_bf16 v[90:93], v[210:213], v[110:113], v[90:93]
	v_mfma_f32_16x16x32_bf16 v[94:97], v[210:213], v[126:129], v[94:97]
	s_nop 7
	v_exp_f32_e32 v66, v66
	v_exp_f32_e32 v67, v67
	v_exp_f32_e32 v68, v68
	v_exp_f32_e32 v69, v69
	v_exp_f32_e32 v70, v70
	v_exp_f32_e32 v71, v71
	v_exp_f32_e32 v72, v72
	v_exp_f32_e32 v73, v73
	v_exp_f32_e32 v74, v74
	v_exp_f32_e32 v75, v75
	v_exp_f32_e32 v76, v76
	v_exp_f32_e32 v77, v77
	v_exp_f32_e32 v78, v78
	v_exp_f32_e32 v79, v79
	v_exp_f32_e32 v80, v80
	v_exp_f32_e32 v81, v81
	v_exp_f32_e32 v82, v82
	v_exp_f32_e32 v83, v83
	v_exp_f32_e32 v84, v84
	v_exp_f32_e32 v85, v85
	v_exp_f32_e32 v86, v86
	v_exp_f32_e32 v87, v87
	v_exp_f32_e32 v88, v88
	v_exp_f32_e32 v89, v89
	v_exp_f32_e32 v90, v90
	v_exp_f32_e32 v91, v91
	v_exp_f32_e32 v92, v92
	v_exp_f32_e32 v93, v93
	v_exp_f32_e32 v94, v94
	v_exp_f32_e32 v95, v95
	v_exp_f32_e32 v96, v96
	v_exp_f32_e32 v97, v97
	v_cvt_pk_bf16_f32 v130, v66, v67
	v_cvt_pk_bf16_f32 v131, v68, v69
	v_cvt_pk_bf16_f32 v132, v74, v75
	v_cvt_pk_bf16_f32 v133, v76, v77
	v_cvt_pk_bf16_f32 v134, v82, v83
	v_cvt_pk_bf16_f32 v135, v84, v85
	v_cvt_pk_bf16_f32 v136, v90, v91
	v_cvt_pk_bf16_f32 v137, v92, v93
	v_cvt_pk_bf16_f32 v138, v70, v71
	v_cvt_pk_bf16_f32 v139, v72, v73
	v_cvt_pk_bf16_f32 v140, v78, v79
	v_cvt_pk_bf16_f32 v141, v80, v81
	v_cvt_pk_bf16_f32 v142, v86, v87
	v_cvt_pk_bf16_f32 v143, v88, v89
	v_cvt_pk_bf16_f32 v144, v94, v95
	v_cvt_pk_bf16_f32 v145, v96, v97
	s_mov_b32 s97, 1
	s_cmp_lt_u32 s42, 4
	s_cbranch_scc1 .Lf16_L_loop
	.p2align 6
.Lf16_N_loop:
	ds_read_b128 v[146:149], v183 offset:32768
	ds_read_b128 v[150:153], v183 offset:36864
	ds_read_b128 v[154:157], v183 offset:40960
	ds_read_b128 v[158:161], v183 offset:45056
	ds_read_b128 v[198:201], v184 offset:32768
	ds_read_b128 v[202:205], v184 offset:36864
	ds_read_b128 v[206:209], v184 offset:40960
	ds_read_b128 v[210:213], v184 offset:45056
	s_waitcnt lgkmcnt(6)
	v_mfma_f32_16x16x32_bf16 v[66:69], v[146:149], v[98:101], 0
	v_mfma_f32_16x16x32_bf16 v[70:73], v[146:149], v[114:117], 0
	v_mfma_f32_16x16x32_bf16 v[74:77], v[150:153], v[98:101], 0
	v_mfma_f32_16x16x32_bf16 v[78:81], v[150:153], v[114:117], 0
	ds_read_b128 v[146:149], v185 offset:32768
	ds_read_b128 v[150:153], v185 offset:36864
	s_waitcnt lgkmcnt(6)
	v_mfma_f32_16x16x32_bf16 v[82:85], v[154:157], v[98:101], 0
	v_mfma_f32_16x16x32_bf16 v[86:89], v[154:157], v[114:117], 0
	v_mfma_f32_16x16x32_bf16 v[90:93], v[158:161], v[98:101], 0
	v_mfma_f32_16x16x32_bf16 v[94:97], v[158:161], v[114:117], 0
	ds_read_b128 v[154:157], v185 offset:40960
	ds_read_b128 v[158:161], v185 offset:45056
	s_waitcnt lgkmcnt(6)
	v_mfma_f32_16x16x32_bf16 v[66:69], v[198:201], v[102:105], v[66:69]
	v_mfma_f32_16x16x32_bf16 v[70:73], v[198:201], v[118:121], v[70:73]
	v_mfma_f32_16x16x32_bf16 v[74:77], v[202:205], v[102:105], v[74:77]
	v_mfma_f32_16x16x32_bf16 v[78:81], v[202:205], v[118:121], v[78:81]
	ds_read_b128 v[198:201], v186 offset:32768
	ds_read_b128 v[202:205], v186 offset:36864
	s_waitcnt lgkmcnt(6)
	v_mfma_f32_16x16x32_bf16 v[82:85], v[206:209], v[102:105], v[82:85]
	v_mfma_f32_16x16x32_bf16 v[86:89], v[206:209], v[118:121], v[86:89]
	v_mfma_f32_16x16x32_bf16 v[90:93], v[210:213], v[102:105], v[90:93]
	v_mfma_f32_16x16x32_bf16 v[94:97], v[210:213], v[118:121], v[94:97]
	ds_read_b128 v[206:209], v186 offset:40960
	ds_read_b128 v[210:213], v186 offset:45056
	s_waitcnt lgkmcnt(6)
	v_mfma_f32_16x16x32_bf16 v[66:69], v[146:149], v[106:109], v[66:69]
	v_mfma_f32_16x16x32_bf16 v[70:73], v[146:149], v[122:125], v[70:73]
	v_mfma_f32_16x16x32_bf16 v[74:77], v[150:153], v[106:109], v[74:77]
	v_mfma_f32_16x16x32_bf16 v[78:81], v[150:153], v[122:125], v[78:81]
	s_waitcnt lgkmcnt(4)
	v_mfma_f32_16x16x32_bf16 v[82:85], v[154:157], v[106:109], v[82:85]
	v_mfma_f32_16x16x32_bf16 v[86:89], v[154:157], v[122:125], v[86:89]
	v_mfma_f32_16x16x32_bf16 v[90:93], v[158:161], v[106:109], v[90:93]
	v_mfma_f32_16x16x32_bf16 v[94:97], v[158:161], v[122:125], v[94:97]
	s_waitcnt lgkmcnt(2)
	v_mfma_f32_16x16x32_bf16 v[66:69], v[198:201], v[110:113], v[66:69]
	v_mfma_f32_16x16x32_bf16 v[70:73], v[198:201], v[126:129], v[70:73]
	v_mfma_f32_16x16x32_bf16 v[74:77], v[202:205], v[110:113], v[74:77]
	v_mfma_f32_16x16x32_bf16 v[78:81], v[202:205], v[126:129], v[78:81]
	ds_read_b64_tr_b16 v[214:215], v191 offset:0
	ds_read_b64_tr_b16 v[216:217], v191 offset:4096
	ds_read_b64_tr_b16 v[218:219], v192 offset:0
	ds_read_b64_tr_b16 v[220:221], v192 offset:4096
	ds_read_b64_tr_b16 v[222:223], v191 offset:512
	ds_read_b64_tr_b16 v[224:225], v191 offset:4608
	ds_read_b64_tr_b16 v[226:227], v192 offset:512
	ds_read_b64_tr_b16 v[228:229], v192 offset:4608
	ds_read_b64_tr_b16 v[230:231], v191 offset:1024
	ds_read_b64_tr_b16 v[232:233], v191 offset:5120
	ds_read_b64_tr_b16 v[234:235], v192 offset:1024
	ds_read_b64_tr_b16 v[236:237], v192 offset:5120
	s_waitcnt lgkmcnt(12)
	v_mfma_f32_16x16x32_bf16 v[82:85], v[206:209], v[110:113], v[82:85]
	v_mfma_f32_16x16x32_bf16 v[86:89], v[206:209], v[126:129], v[86:89]
	v_mfma_f32_16x16x32_bf16 v[90:93], v[210:213], v[110:113], v[90:93]
	v_mfma_f32_16x16x32_bf16 v[94:97], v[210:213], v[126:129], v[94:97]
	s_waitcnt vmcnt(0) lgkmcnt(0)
	s_barrier
; #define SBAR() __builtin_amdgcn_sched_barrier(0)
; #define RESC(a) do { if (__any((a) < 1.f)) { if (hi == 0) al_l[r32] = (a); asm volatile("s_waitcnt lgkmcnt(0)" ::: "memory"); \
;     for (int d = 0; d < 4; ++d) for (int r = 0; r < 16; ++r) o[d][r] *= al_l[crow(r, hi)]; } } while (0)
; #define RESC(a) do { if (__any((a) < 1.f)) { if (hi == 0) al_l[r32] = (a); asm volatile("s_waitcnt lgkmcnt(0)" ::: "memory"); \
;     for (int d = 0; d < 4; ++d) for (int r = 0; r < 16; ++r) o[d][r] *= al_l[crow(r, hi)]; } } while (0)
; #define ATT_SYNC(jn) do { ATT_WAIT_BAR(); if ((jn) < NT) ATT_DMA((jn), (jn) & 3); } while (0)
; __device__ __forceinline__ void pv_d0(f32x16* o, int vb, bf16x8 pa0, bf16x8 pa1, bf16x8 pa2, bf16x8 pa3) {
;   s16x4 ra[8], rb[8];
;   pv_rd<0>(ra, vb); pv_rd<1>(rb, vb);
;   asm volatile("s_waitcnt lgkmcnt(8)" ::: "memory"); SBAR(); pv_mm(o[0], ra, pa0, pa1, pa2, pa3); pv_rd<2>(ra, vb);
;   asm volatile("s_waitcnt lgkmcnt(8)" ::: "memory"); SBAR(); pv_mm(o[1], rb, pa0, pa1, pa2, pa3); pv_rd<3>(rb, vb);
;   asm volatile("s_waitcnt lgkmcnt(8)" ::: "memory"); SBAR(); pv_mm(o[2], ra, pa0, pa1, pa2, pa3);
;   asm volatile("s_waitcnt lgkmcnt(0)" ::: "memory"); SBAR(); pv_mm(o[3], rb, pa0, pa1, pa2, pa3);
; }
; __device__ __forceinline__ void attn_dma_body(const bf16_t* __restrict__ Qb, int ldq, int tpos0, const float* __restrict__ rope, const float* __restrict__ qgain, ...
;     ...
;   for (int j = 1; j + 1 < NT; j += 2) {
;     { SBAR(); qkt(pB0, pB1, (const bf16_t*)(lds + (j & 3) * SHM_SLOT), qr, r32, hi);
;       finishSM(pA0, pA1, alA, l_reg, pa0, pa1, pa2, pa3); s16x4 va[8]; pv_rd<0>(va, vb0 + ((j - 1) & 3) * (int)SHM_SLOT); SBAR();
;       if (!lead) ATT_SYNC(j + 2);
;       pv_d0_pre(o, vb0 + ((j - 1) & 3) * (int)SHM_SLOT, va, pa0, pa1, pa2, pa3); partialSM(pB0, pB1, m_reg, mnB, alB);
;       if (lead) ATT_SYNC(j + 2);
;       RESC(alB); }
;     { SBAR(); qkt(pA0, pA1, (const bf16_t*)(lds + ((j + 1) & 3) * SHM_SLOT), qr, r32, hi);
;       finishSM(pB0, pB1, alB, l_reg, pa0, pa1, pa2, pa3); s16x4 va[8]; pv_rd<0>(va, vb0 + (j & 3) * (int)SHM_SLOT); SBAR();
;       if (!lead) ATT_SYNC(j + 3);
;       pv_d0_pre(o, vb0 + (j & 3) * (int)SHM_SLOT, va, pa0, pa1, pa2, pa3); partialSM(pA0, pA1, m_reg, mnA, alA);
;       if (lead) ATT_SYNC(j + 3);
;       RESC(alA); }
;   }
	s_cmp_ge_u32 s97, 130
	s_cbranch_scc1 .Lf16_se_N0
	s_add_i32 m0, s96, 0x18000
	s_nop 0
	global_load_lds_dwordx4 v170, s[2:3]
	s_add_i32 m0, s96, 0x1a000
	s_nop 0
	global_load_lds_dwordx4 v172, s[2:3]
	s_add_i32 m0, s96, 0x1c000
	s_nop 0
	global_load_lds_dwordx4 v171, s[2:3]
	s_add_i32 m0, s96, 0x1e000
	s_nop 0
	global_load_lds_dwordx4 v173, s[2:3]
	s_add_u32 s2, s2, 0x4000
	s_addc_u32 s3, s3, 0
.Lf16_se_N0:
	s_waitcnt lgkmcnt(8)
	v_mfma_f32_16x16x32_bf16 v[2:5], v[214:217], v[130:133], v[2:5]
	v_exp_f32_e32 v66, v66
	v_mfma_f32_16x16x32_bf16 v[6:9], v[214:217], v[138:141], v[6:9]
	v_exp_f32_e32 v67, v67
	v_mfma_f32_16x16x32_bf16 v[10:13], v[218:221], v[130:133], v[10:13]
	v_exp_f32_e32 v68, v68
	v_mfma_f32_16x16x32_bf16 v[14:17], v[218:221], v[138:141], v[14:17]
	v_exp_f32_e32 v69, v69
	ds_read_b64_tr_b16 v[238:239], v191 offset:1536
	ds_read_b64_tr_b16 v[240:241], v191 offset:5632
	ds_read_b64_tr_b16 v[242:243], v192 offset:1536
	ds_read_b64_tr_b16 v[244:245], v192 offset:5632
	s_waitcnt lgkmcnt(8)
	v_mfma_f32_16x16x32_bf16 v[18:21], v[222:225], v[130:133], v[18:21]
	v_exp_f32_e32 v70, v70
	v_mfma_f32_16x16x32_bf16 v[22:25], v[222:225], v[138:141], v[22:25]
	v_exp_f32_e32 v71, v71
	v_mfma_f32_16x16x32_bf16 v[26:29], v[226:229], v[130:133], v[26:29]
	v_exp_f32_e32 v72, v72
	v_mfma_f32_16x16x32_bf16 v[30:33], v[226:229], v[138:141], v[30:33]
	v_exp_f32_e32 v73, v73
	v_mfma_f32_16x16x32_bf16 v[246:249], v[194:197], v[130:133], v[246:249]
	ds_read_b64_tr_b16 v[214:215], v191 offset:8192
	ds_read_b64_tr_b16 v[216:217], v191 offset:12288
	ds_read_b64_tr_b16 v[218:219], v192 offset:8192
	ds_read_b64_tr_b16 v[220:221], v192 offset:12288
	s_waitcnt lgkmcnt(8)
	v_mfma_f32_16x16x32_bf16 v[34:37], v[230:233], v[130:133], v[34:37]
	v_exp_f32_e32 v74, v74
	v_mfma_f32_16x16x32_bf16 v[38:41], v[230:233], v[138:141], v[38:41]
	v_exp_f32_e32 v75, v75
	v_mfma_f32_16x16x32_bf16 v[42:45], v[234:237], v[130:133], v[42:45]
	v_exp_f32_e32 v76, v76
	v_mfma_f32_16x16x32_bf16 v[46:49], v[234:237], v[138:141], v[46:49]
	v_exp_f32_e32 v77, v77
	ds_read_b64_tr_b16 v[222:223], v191 offset:8704
	ds_read_b64_tr_b16 v[224:225], v191 offset:12800
	ds_read_b64_tr_b16 v[226:227], v192 offset:8704
	ds_read_b64_tr_b16 v[228:229], v192 offset:12800
	s_waitcnt lgkmcnt(8)
	v_mfma_f32_16x16x32_bf16 v[50:53], v[238:241], v[130:133], v[50:53]
	v_exp_f32_e32 v78, v78
	v_mfma_f32_16x16x32_bf16 v[54:57], v[238:241], v[138:141], v[54:57]
	v_exp_f32_e32 v79, v79
	v_mfma_f32_16x16x32_bf16 v[58:61], v[242:245], v[130:133], v[58:61]
	v_exp_f32_e32 v80, v80
	v_mfma_f32_16x16x32_bf16 v[62:65], v[242:245], v[138:141], v[62:65]
	v_exp_f32_e32 v81, v81
	v_mfma_f32_16x16x32_bf16 v[252:255], v[194:197], v[138:141], v[252:255]
	ds_read_b64_tr_b16 v[230:231], v191 offset:9216
	ds_read_b64_tr_b16 v[232:233], v191 offset:13312
	ds_read_b64_tr_b16 v[234:235], v192 offset:9216
	ds_read_b64_tr_b16 v[236:237], v192 offset:13312
	s_waitcnt lgkmcnt(8)
	v_mfma_f32_16x16x32_bf16 v[2:5], v[214:217], v[134:137], v[2:5]
	v_exp_f32_e32 v82, v82
	v_mfma_f32_16x16x32_bf16 v[6:9], v[214:217], v[142:145], v[6:9]
	v_exp_f32_e32 v83, v83
	v_mfma_f32_16x16x32_bf16 v[10:13], v[218:221], v[134:137], v[10:13]
	v_exp_f32_e32 v84, v84
	v_mfma_f32_16x16x32_bf16 v[14:17], v[218:221], v[142:145], v[14:17]
	v_exp_f32_e32 v85, v85
	ds_read_b64_tr_b16 v[238:239], v191 offset:9728
	ds_read_b64_tr_b16 v[240:241], v191 offset:13824
	ds_read_b64_tr_b16 v[242:243], v192 offset:9728
	ds_read_b64_tr_b16 v[244:245], v192 offset:13824
	s_waitcnt lgkmcnt(8)
	v_mfma_f32_16x16x32_bf16 v[18:21], v[222:225], v[134:137], v[18:21]
	v_exp_f32_e32 v86, v86
	v_mfma_f32_16x16x32_bf16 v[22:25], v[222:225], v[142:145], v[22:25]
	v_exp_f32_e32 v87, v87
	v_mfma_f32_16x16x32_bf16 v[26:29], v[226:229], v[134:137], v[26:29]
	v_exp_f32_e32 v88, v88
	v_mfma_f32_16x16x32_bf16 v[30:33], v[226:229], v[142:145], v[30:33]
	v_exp_f32_e32 v89, v89
	v_mfma_f32_16x16x32_bf16 v[246:249], v[194:197], v[134:137], v[246:249]
	s_waitcnt lgkmcnt(4)
	v_mfma_f32_16x16x32_bf16 v[34:37], v[230:233], v[134:137], v[34:37]
	v_exp_f32_e32 v90, v90
	v_mfma_f32_16x16x32_bf16 v[38:41], v[230:233], v[142:145], v[38:41]
	v_exp_f32_e32 v91, v91
	v_mfma_f32_16x16x32_bf16 v[42:45], v[234:237], v[134:137], v[42:45]
	v_exp_f32_e32 v92, v92
	v_mfma_f32_16x16x32_bf16 v[46:49], v[234:237], v[142:145], v[46:49]
	v_exp_f32_e32 v93, v93
	s_waitcnt lgkmcnt(0)
	v_mfma_f32_16x16x32_bf16 v[50:53], v[238:241], v[134:137], v[50:53]
	v_exp_f32_e32 v94, v94
	v_mfma_f32_16x16x32_bf16 v[54:57], v[238:241], v[142:145], v[54:57]
	v_exp_f32_e32 v95, v95
	v_mfma_f32_16x16x32_bf16 v[58:61], v[242:245], v[134:137], v[58:61]
	v_exp_f32_e32 v96, v96
	v_mfma_f32_16x16x32_bf16 v[62:65], v[242:245], v[142:145], v[62:65]
	v_exp_f32_e32 v97, v97
	v_mfma_f32_16x16x32_bf16 v[252:255], v[194:197], v[142:145], v[252:255]
	v_cvt_pk_bf16_f32 v130, v66, v67
	v_cvt_pk_bf16_f32 v131, v68, v69
	v_cvt_pk_bf16_f32 v132, v74, v75
	v_cvt_pk_bf16_f32 v133, v76, v77
	v_cvt_pk_bf16_f32 v134, v82, v83
	v_cvt_pk_bf16_f32 v135, v84, v85
	v_cvt_pk_bf16_f32 v136, v90, v91
	v_cvt_pk_bf16_f32 v137, v92, v93
	v_cvt_pk_bf16_f32 v138, v70, v71
	v_cvt_pk_bf16_f32 v139, v72, v73
	v_cvt_pk_bf16_f32 v140, v78, v79
	v_cvt_pk_bf16_f32 v141, v80, v81
	v_cvt_pk_bf16_f32 v142, v86, v87
	v_cvt_pk_bf16_f32 v143, v88, v89
	v_cvt_pk_bf16_f32 v144, v94, v95
	v_cvt_pk_bf16_f32 v145, v96, v97
	s_add_i32 s97, s97, 1
	ds_read_b128 v[146:149], v187 offset:0
	ds_read_b128 v[150:153], v187 offset:4096
	ds_read_b128 v[154:157], v187 offset:8192
	ds_read_b128 v[158:161], v187 offset:12288
	ds_read_b128 v[198:201], v188 offset:0
	ds_read_b128 v[202:205], v188 offset:4096
	ds_read_b128 v[206:209], v188 offset:8192
	ds_read_b128 v[210:213], v188 offset:12288
	s_waitcnt lgkmcnt(6)
; template <int D0> __device__ __forceinline__ void pv_rd(s16x4 (&r)[8], int vb) {
;   r[0] = tr_read<v_rd_off(D0, 0, 0)>(vb); r[1] = tr_read<v_rd_off(D0, 0, 1)>(vb); r[2] = tr_read<v_rd_off(D0, 1, 0)>(vb); r[3] = tr_read<v_rd_off(D0, 1, 1)>(vb);
;   r[4] = tr_read<v_rd_off(D0, 2, 0)>(vb); r[5] = tr_read<v_rd_off(D0, 2, 1)>(vb); r[6] = tr_read<v_rd_off(D0, 3, 0)>(vb); r[7] = tr_read<v_rd_off(D0, 3, 1)>(vb);
; }
; __device__ __forceinline__ void pv_mm(f32x16& od, const s16x4 (&r)[8], bf16x8 pa0, bf16x8 pa1, bf16x8 pa2, bf16x8 pa3) {
;     ...
;   od = __builtin_amdgcn_mfma_f32_32x32x16_bf16(pa0, PK(r[0], r[1]), od, 0, 0, 0);
;   od = __builtin_amdgcn_mfma_f32_32x32x16_bf16(pa1, PK(r[2], r[3]), od, 0, 0, 0);
;   od = __builtin_amdgcn_mfma_f32_32x32x16_bf16(pa2, PK(r[4], r[5]), od, 0, 0, 0);
;   od = __builtin_amdgcn_mfma_f32_32x32x16_bf16(pa3, PK(r[6], r[7]), od, 0, 0, 0);
;     ...
; }
; __device__ __forceinline__ void pv_d0(f32x16* o, int vb, bf16x8 pa0, bf16x8 pa1, bf16x8 pa2, bf16x8 pa3) {
;   s16x4 ra[8], rb[8];
;   pv_rd<0>(ra, vb); pv_rd<1>(rb, vb);
;   asm volatile("s_waitcnt lgkmcnt(8)" ::: "memory"); SBAR(); pv_mm(o[0], ra, pa0, pa1, pa2, pa3); pv_rd<2>(ra, vb);
;   asm volatile("s_waitcnt lgkmcnt(8)" ::: "memory"); SBAR(); pv_mm(o[1], rb, pa0, pa1, pa2, pa3); pv_rd<3>(rb, vb);
; __device__ __forceinline__ void attn_dma_body(const bf16_t* __restrict__ Qb, int ldq, int tpos0, const float* __restrict__ rope, const float* __restrict__ qgain, ...
;     ...
;   for (int j = 1; j + 1 < NT; j += 2) {
;     { SBAR(); qkt(pB0, pB1, (const bf16_t*)(lds + (j & 3) * SHM_SLOT), qr, r32, hi);
;       finishSM(pA0, pA1, alA, l_reg, pa0, pa1, pa2, pa3); s16x4 va[8]; pv_rd<0>(va, vb0 + ((j - 1) & 3) * (int)SHM_SLOT); SBAR();
;       if (!lead) ATT_SYNC(j + 2);
;       pv_d0_pre(o, vb0 + ((j - 1) & 3) * (int)SHM_SLOT, va, pa0, pa1, pa2, pa3); partialSM(pB0, pB1, m_reg, mnB, alB);
;       if (lead) ATT_SYNC(j + 2);
;       RESC(alB); }
;     { SBAR(); qkt(pA0, pA1, (const bf16_t*)(lds + ((j + 1) & 3) * SHM_SLOT), qr, r32, hi);
;       finishSM(pB0, pB1, alB, l_reg, pa0, pa1, pa2, pa3); s16x4 va[8]; pv_rd<0>(va, vb0 + (j & 3) * (int)SHM_SLOT); SBAR();
;       if (!lead) ATT_SYNC(j + 3);
;       pv_d0_pre(o, vb0 + (j & 3) * (int)SHM_SLOT, va, pa0, pa1, pa2, pa3); partialSM(pA0, pA1, m_reg, mnA, alA);
;       if (lead) ATT_SYNC(j + 3);
;       RESC(alA); }
;   }
	v_mfma_f32_16x16x32_bf16 v[66:69], v[146:149], v[98:101], 0
	v_mfma_f32_16x16x32_bf16 v[70:73], v[146:149], v[114:117], 0
	v_mfma_f32_16x16x32_bf16 v[74:77], v[150:153], v[98:101], 0
	v_mfma_f32_16x16x32_bf16 v[78:81], v[150:153], v[114:117], 0
	ds_read_b128 v[146:149], v189 offset:0
	ds_read_b128 v[150:153], v189 offset:4096
	s_waitcnt lgkmcnt(6)
	v_mfma_f32_16x16x32_bf16 v[82:85], v[154:157], v[98:101], 0
	v_mfma_f32_16x16x32_bf16 v[86:89], v[154:157], v[114:117], 0
	v_mfma_f32_16x16x32_bf16 v[90:93], v[158:161], v[98:101], 0
	v_mfma_f32_16x16x32_bf16 v[94:97], v[158:161], v[114:117], 0
	ds_read_b128 v[154:157], v189 offset:8192
	ds_read_b128 v[158:161], v189 offset:12288
	s_waitcnt lgkmcnt(6)
	v_mfma_f32_16x16x32_bf16 v[66:69], v[198:201], v[102:105], v[66:69]
	v_mfma_f32_16x16x32_bf16 v[70:73], v[198:201], v[118:121], v[70:73]
	v_mfma_f32_16x16x32_bf16 v[74:77], v[202:205], v[102:105], v[74:77]
	v_mfma_f32_16x16x32_bf16 v[78:81], v[202:205], v[118:121], v[78:81]
	ds_read_b128 v[198:201], v190 offset:0
	ds_read_b128 v[202:205], v190 offset:4096
	s_waitcnt lgkmcnt(6)
	v_mfma_f32_16x16x32_bf16 v[82:85], v[206:209], v[102:105], v[82:85]
	v_mfma_f32_16x16x32_bf16 v[86:89], v[206:209], v[118:121], v[86:89]
	v_mfma_f32_16x16x32_bf16 v[90:93], v[210:213], v[102:105], v[90:93]
	v_mfma_f32_16x16x32_bf16 v[94:97], v[210:213], v[118:121], v[94:97]
	ds_read_b128 v[206:209], v190 offset:8192
	ds_read_b128 v[210:213], v190 offset:12288
	s_waitcnt lgkmcnt(6)
	v_mfma_f32_16x16x32_bf16 v[66:69], v[146:149], v[106:109], v[66:69]
	v_mfma_f32_16x16x32_bf16 v[70:73], v[146:149], v[122:125], v[70:73]
	v_mfma_f32_16x16x32_bf16 v[74:77], v[150:153], v[106:109], v[74:77]
	v_mfma_f32_16x16x32_bf16 v[78:81], v[150:153], v[122:125], v[78:81]
	s_waitcnt lgkmcnt(4)
	v_mfma_f32_16x16x32_bf16 v[82:85], v[154:157], v[106:109], v[82:85]
	v_mfma_f32_16x16x32_bf16 v[86:89], v[154:157], v[122:125], v[86:89]
	v_mfma_f32_16x16x32_bf16 v[90:93], v[158:161], v[106:109], v[90:93]
	v_mfma_f32_16x16x32_bf16 v[94:97], v[158:161], v[122:125], v[94:97]
	s_waitcnt lgkmcnt(2)
	v_mfma_f32_16x16x32_bf16 v[66:69], v[198:201], v[110:113], v[66:69]
	v_mfma_f32_16x16x32_bf16 v[70:73], v[198:201], v[126:129], v[70:73]
	v_mfma_f32_16x16x32_bf16 v[74:77], v[202:205], v[110:113], v[74:77]
	v_mfma_f32_16x16x32_bf16 v[78:81], v[202:205], v[126:129], v[78:81]
	ds_read_b64_tr_b16 v[214:215], v191 offset:32768
	ds_read_b64_tr_b16 v[216:217], v191 offset:36864
	ds_read_b64_tr_b16 v[218:219], v192 offset:32768
	ds_read_b64_tr_b16 v[220:221], v192 offset:36864
	ds_read_b64_tr_b16 v[222:223], v191 offset:33280
	ds_read_b64_tr_b16 v[224:225], v191 offset:37376
	ds_read_b64_tr_b16 v[226:227], v192 offset:33280
	ds_read_b64_tr_b16 v[228:229], v192 offset:37376
	ds_read_b64_tr_b16 v[230:231], v191 offset:33792
	ds_read_b64_tr_b16 v[232:233], v191 offset:37888
	ds_read_b64_tr_b16 v[234:235], v192 offset:33792
	ds_read_b64_tr_b16 v[236:237], v192 offset:37888
	s_waitcnt lgkmcnt(12)
	v_mfma_f32_16x16x32_bf16 v[82:85], v[206:209], v[110:113], v[82:85]
	v_mfma_f32_16x16x32_bf16 v[86:89], v[206:209], v[126:129], v[86:89]
	v_mfma_f32_16x16x32_bf16 v[90:93], v[210:213], v[110:113], v[90:93]
	v_mfma_f32_16x16x32_bf16 v[94:97], v[210:213], v[126:129], v[94:97]
	s_waitcnt vmcnt(0) lgkmcnt(0)
	s_barrier
	s_cmp_ge_u32 s97, 130
	s_cbranch_scc1 .Lf16_se_N1
	s_add_i32 m0, s96, 0x0
	s_nop 0
	global_load_lds_dwordx4 v170, s[2:3]
	s_add_i32 m0, s96, 0x2000
	s_nop 0
	global_load_lds_dwordx4 v172, s[2:3]
	s_add_i32 m0, s96, 0x4000
	s_nop 0
	global_load_lds_dwordx4 v171, s[2:3]
	s_add_i32 m0, s96, 0x6000
	s_nop 0
	global_load_lds_dwordx4 v173, s[2:3]
	s_add_u32 s2, s2, 0x4000
	s_addc_u32 s3, s3, 0
.Lf16_se_N1:
	s_waitcnt lgkmcnt(8)
	v_mfma_f32_16x16x32_bf16 v[2:5], v[214:217], v[130:133], v[2:5]
	v_exp_f32_e32 v66, v66
	v_mfma_f32_16x16x32_bf16 v[6:9], v[214:217], v[138:141], v[6:9]
	v_exp_f32_e32 v67, v67
	v_mfma_f32_16x16x32_bf16 v[10:13], v[218:221], v[130:133], v[10:13]
	v_exp_f32_e32 v68, v68
	v_mfma_f32_16x16x32_bf16 v[14:17], v[218:221], v[138:141], v[14:17]
	v_exp_f32_e32 v69, v69
	ds_read_b64_tr_b16 v[238:239], v191 offset:34304
	ds_read_b64_tr_b16 v[240:241], v191 offset:38400
	ds_read_b64_tr_b16 v[242:243], v192 offset:34304
	ds_read_b64_tr_b16 v[244:245], v192 offset:38400
	s_waitcnt lgkmcnt(8)
	v_mfma_f32_16x16x32_bf16 v[18:21], v[222:225], v[130:133], v[18:21]
	v_exp_f32_e32 v70, v70
	v_mfma_f32_16x16x32_bf16 v[22:25], v[222:225], v[138:141], v[22:25]
	v_exp_f32_e32 v71, v71
	v_mfma_f32_16x16x32_bf16 v[26:29], v[226:229], v[130:133], v[26:29]
	v_exp_f32_e32 v72, v72
	v_mfma_f32_16x16x32_bf16 v[30:33], v[226:229], v[138:141], v[30:33]
	v_exp_f32_e32 v73, v73
	v_mfma_f32_16x16x32_bf16 v[246:249], v[194:197], v[130:133], v[246:249]
	ds_read_b64_tr_b16 v[214:215], v191 offset:40960
	ds_read_b64_tr_b16 v[216:217], v191 offset:45056
	ds_read_b64_tr_b16 v[218:219], v192 offset:40960
	ds_read_b64_tr_b16 v[220:221], v192 offset:45056
	s_waitcnt lgkmcnt(8)
	v_mfma_f32_16x16x32_bf16 v[34:37], v[230:233], v[130:133], v[34:37]
	v_exp_f32_e32 v74, v74
	v_mfma_f32_16x16x32_bf16 v[38:41], v[230:233], v[138:141], v[38:41]
	v_exp_f32_e32 v75, v75
	v_mfma_f32_16x16x32_bf16 v[42:45], v[234:237], v[130:133], v[42:45]
	v_exp_f32_e32 v76, v76
	v_mfma_f32_16x16x32_bf16 v[46:49], v[234:237], v[138:141], v[46:49]
	v_exp_f32_e32 v77, v77
	ds_read_b64_tr_b16 v[222:223], v191 offset:41472
	ds_read_b64_tr_b16 v[224:225], v191 offset:45568
	ds_read_b64_tr_b16 v[226:227], v192 offset:41472
	ds_read_b64_tr_b16 v[228:229], v192 offset:45568
	s_waitcnt lgkmcnt(8)
; #define SBAR() __builtin_amdgcn_sched_barrier(0)
; #define RESC(a) do { if (__any((a) < 1.f)) { if (hi == 0) al_l[r32] = (a); asm volatile("s_waitcnt lgkmcnt(0)" ::: "memory"); \
;     for (int d = 0; d < 4; ++d) for (int r = 0; r < 16; ++r) o[d][r] *= al_l[crow(r, hi)]; } } while (0)
; #define RESC(a) do { if (__any((a) < 1.f)) { if (hi == 0) al_l[r32] = (a); asm volatile("s_waitcnt lgkmcnt(0)" ::: "memory"); \
;     for (int d = 0; d < 4; ++d) for (int r = 0; r < 16; ++r) o[d][r] *= al_l[crow(r, hi)]; } } while (0)
; #define ATT_SYNC(jn) do { ATT_WAIT_BAR(); if ((jn) < NT) ATT_DMA((jn), (jn) & 3); } while (0)
; __device__ __forceinline__ void attn_dma_body(const bf16_t* __restrict__ Qb, int ldq, int tpos0, const float* __restrict__ rope, const float* __restrict__ qgain, ...
;     ...
;   for (int j = 1; j + 1 < NT; j += 2) {
;     { SBAR(); qkt(pB0, pB1, (const bf16_t*)(lds + (j & 3) * SHM_SLOT), qr, r32, hi);
;       finishSM(pA0, pA1, alA, l_reg, pa0, pa1, pa2, pa3); s16x4 va[8]; pv_rd<0>(va, vb0 + ((j - 1) & 3) * (int)SHM_SLOT); SBAR();
;       if (!lead) ATT_SYNC(j + 2);
;       pv_d0_pre(o, vb0 + ((j - 1) & 3) * (int)SHM_SLOT, va, pa0, pa1, pa2, pa3); partialSM(pB0, pB1, m_reg, mnB, alB);
;       if (lead) ATT_SYNC(j + 2);
;       RESC(alB); }
;     { SBAR(); qkt(pA0, pA1, (const bf16_t*)(lds + ((j + 1) & 3) * SHM_SLOT), qr, r32, hi);
;       finishSM(pB0, pB1, alB, l_reg, pa0, pa1, pa2, pa3); s16x4 va[8]; pv_rd<0>(va, vb0 + (j & 3) * (int)SHM_SLOT); SBAR();
;       if (!lead) ATT_SYNC(j + 3);
;       pv_d0_pre(o, vb0 + (j & 3) * (int)SHM_SLOT, va, pa0, pa1, pa2, pa3); partialSM(pA0, pA1, m_reg, mnA, alA);
;       if (lead) ATT_SYNC(j + 3);
;       RESC(alA); }
;   }
	v_mfma_f32_16x16x32_bf16 v[50:53], v[238:241], v[130:133], v[50:53]
	v_exp_f32_e32 v78, v78
	v_mfma_f32_16x16x32_bf16 v[54:57], v[238:241], v[138:141], v[54:57]
	v_exp_f32_e32 v79, v79
	v_mfma_f32_16x16x32_bf16 v[58:61], v[242:245], v[130:133], v[58:61]
	v_exp_f32_e32 v80, v80
	v_mfma_f32_16x16x32_bf16 v[62:65], v[242:245], v[138:141], v[62:65]
	v_exp_f32_e32 v81, v81
	v_mfma_f32_16x16x32_bf16 v[252:255], v[194:197], v[138:141], v[252:255]
	ds_read_b64_tr_b16 v[230:231], v191 offset:41984
	ds_read_b64_tr_b16 v[232:233], v191 offset:46080
	ds_read_b64_tr_b16 v[234:235], v192 offset:41984
	ds_read_b64_tr_b16 v[236:237], v192 offset:46080
	s_waitcnt lgkmcnt(8)
	v_mfma_f32_16x16x32_bf16 v[2:5], v[214:217], v[134:137], v[2:5]
	v_exp_f32_e32 v82, v82
	v_mfma_f32_16x16x32_bf16 v[6:9], v[214:217], v[142:145], v[6:9]
	v_exp_f32_e32 v83, v83
	v_mfma_f32_16x16x32_bf16 v[10:13], v[218:221], v[134:137], v[10:13]
	v_exp_f32_e32 v84, v84
	v_mfma_f32_16x16x32_bf16 v[14:17], v[218:221], v[142:145], v[14:17]
	v_exp_f32_e32 v85, v85
	ds_read_b64_tr_b16 v[238:239], v191 offset:42496
	ds_read_b64_tr_b16 v[240:241], v191 offset:46592
	ds_read_b64_tr_b16 v[242:243], v192 offset:42496
	ds_read_b64_tr_b16 v[244:245], v192 offset:46592
	s_waitcnt lgkmcnt(8)
	v_mfma_f32_16x16x32_bf16 v[18:21], v[222:225], v[134:137], v[18:21]
	v_exp_f32_e32 v86, v86
	v_mfma_f32_16x16x32_bf16 v[22:25], v[222:225], v[142:145], v[22:25]
	v_exp_f32_e32 v87, v87
	v_mfma_f32_16x16x32_bf16 v[26:29], v[226:229], v[134:137], v[26:29]
	v_exp_f32_e32 v88, v88
	v_mfma_f32_16x16x32_bf16 v[30:33], v[226:229], v[142:145], v[30:33]
	v_exp_f32_e32 v89, v89
	v_mfma_f32_16x16x32_bf16 v[246:249], v[194:197], v[134:137], v[246:249]
	s_waitcnt lgkmcnt(4)
	v_mfma_f32_16x16x32_bf16 v[34:37], v[230:233], v[134:137], v[34:37]
	v_exp_f32_e32 v90, v90
	v_mfma_f32_16x16x32_bf16 v[38:41], v[230:233], v[142:145], v[38:41]
	v_exp_f32_e32 v91, v91
	v_mfma_f32_16x16x32_bf16 v[42:45], v[234:237], v[134:137], v[42:45]
	v_exp_f32_e32 v92, v92
	v_mfma_f32_16x16x32_bf16 v[46:49], v[234:237], v[142:145], v[46:49]
	v_exp_f32_e32 v93, v93
	s_waitcnt lgkmcnt(0)
	v_mfma_f32_16x16x32_bf16 v[50:53], v[238:241], v[134:137], v[50:53]
	v_exp_f32_e32 v94, v94
	v_mfma_f32_16x16x32_bf16 v[54:57], v[238:241], v[142:145], v[54:57]
	v_exp_f32_e32 v95, v95
	v_mfma_f32_16x16x32_bf16 v[58:61], v[242:245], v[134:137], v[58:61]
	v_exp_f32_e32 v96, v96
	v_mfma_f32_16x16x32_bf16 v[62:65], v[242:245], v[142:145], v[62:65]
	v_exp_f32_e32 v97, v97
	v_mfma_f32_16x16x32_bf16 v[252:255], v[194:197], v[142:145], v[252:255]
	v_cvt_pk_bf16_f32 v130, v66, v67
	v_cvt_pk_bf16_f32 v131, v68, v69
	v_cvt_pk_bf16_f32 v132, v74, v75
	v_cvt_pk_bf16_f32 v133, v76, v77
	v_cvt_pk_bf16_f32 v134, v82, v83
	v_cvt_pk_bf16_f32 v135, v84, v85
	v_cvt_pk_bf16_f32 v136, v90, v91
	v_cvt_pk_bf16_f32 v137, v92, v93
	v_cvt_pk_bf16_f32 v138, v70, v71
	v_cvt_pk_bf16_f32 v139, v72, v73
	v_cvt_pk_bf16_f32 v140, v78, v79
	v_cvt_pk_bf16_f32 v141, v80, v81
	v_cvt_pk_bf16_f32 v142, v86, v87
	v_cvt_pk_bf16_f32 v143, v88, v89
	v_cvt_pk_bf16_f32 v144, v94, v95
	v_cvt_pk_bf16_f32 v145, v96, v97
	s_add_i32 s97, s97, 1
	ds_read_b128 v[146:149], v187 offset:32768
	ds_read_b128 v[150:153], v187 offset:36864
	ds_read_b128 v[154:157], v187 offset:40960
	ds_read_b128 v[158:161], v187 offset:45056
	ds_read_b128 v[198:201], v188 offset:32768
	ds_read_b128 v[202:205], v188 offset:36864
	ds_read_b128 v[206:209], v188 offset:40960
	ds_read_b128 v[210:213], v188 offset:45056
	s_waitcnt lgkmcnt(6)
	v_mfma_f32_16x16x32_bf16 v[66:69], v[146:149], v[98:101], 0
	v_mfma_f32_16x16x32_bf16 v[70:73], v[146:149], v[114:117], 0
	v_mfma_f32_16x16x32_bf16 v[74:77], v[150:153], v[98:101], 0
	v_mfma_f32_16x16x32_bf16 v[78:81], v[150:153], v[114:117], 0
	ds_read_b128 v[146:149], v189 offset:32768
	ds_read_b128 v[150:153], v189 offset:36864
	s_waitcnt lgkmcnt(6)
	v_mfma_f32_16x16x32_bf16 v[82:85], v[154:157], v[98:101], 0
	v_mfma_f32_16x16x32_bf16 v[86:89], v[154:157], v[114:117], 0
	v_mfma_f32_16x16x32_bf16 v[90:93], v[158:161], v[98:101], 0
	v_mfma_f32_16x16x32_bf16 v[94:97], v[158:161], v[114:117], 0
	ds_read_b128 v[154:157], v189 offset:40960
	ds_read_b128 v[158:161], v189 offset:45056
	s_waitcnt lgkmcnt(6)
	v_mfma_f32_16x16x32_bf16 v[66:69], v[198:201], v[102:105], v[66:69]
	v_mfma_f32_16x16x32_bf16 v[70:73], v[198:201], v[118:121], v[70:73]
	v_mfma_f32_16x16x32_bf16 v[74:77], v[202:205], v[102:105], v[74:77]
	v_mfma_f32_16x16x32_bf16 v[78:81], v[202:205], v[118:121], v[78:81]
	ds_read_b128 v[198:201], v190 offset:32768
	ds_read_b128 v[202:205], v190 offset:36864
	s_waitcnt lgkmcnt(6)
	v_mfma_f32_16x16x32_bf16 v[82:85], v[206:209], v[102:105], v[82:85]
	v_mfma_f32_16x16x32_bf16 v[86:89], v[206:209], v[118:121], v[86:89]
	v_mfma_f32_16x16x32_bf16 v[90:93], v[210:213], v[102:105], v[90:93]
	v_mfma_f32_16x16x32_bf16 v[94:97], v[210:213], v[118:121], v[94:97]
	ds_read_b128 v[206:209], v190 offset:40960
	ds_read_b128 v[210:213], v190 offset:45056
	s_waitcnt lgkmcnt(6)
	v_mfma_f32_16x16x32_bf16 v[66:69], v[146:149], v[106:109], v[66:69]
	v_mfma_f32_16x16x32_bf16 v[70:73], v[146:149], v[122:125], v[70:73]
	v_mfma_f32_16x16x32_bf16 v[74:77], v[150:153], v[106:109], v[74:77]
	v_mfma_f32_16x16x32_bf16 v[78:81], v[150:153], v[122:125], v[78:81]
	s_waitcnt lgkmcnt(4)
	v_mfma_f32_16x16x32_bf16 v[82:85], v[154:157], v[106:109], v[82:85]
	v_mfma_f32_16x16x32_bf16 v[86:89], v[154:157], v[122:125], v[86:89]
	v_mfma_f32_16x16x32_bf16 v[90:93], v[158:161], v[106:109], v[90:93]
	v_mfma_f32_16x16x32_bf16 v[94:97], v[158:161], v[122:125], v[94:97]
	s_waitcnt lgkmcnt(2)
	v_mfma_f32_16x16x32_bf16 v[66:69], v[198:201], v[110:113], v[66:69]
	v_mfma_f32_16x16x32_bf16 v[70:73], v[198:201], v[126:129], v[70:73]
	v_mfma_f32_16x16x32_bf16 v[74:77], v[202:205], v[110:113], v[74:77]
	v_mfma_f32_16x16x32_bf16 v[78:81], v[202:205], v[126:129], v[78:81]
	ds_read_b64_tr_b16 v[214:215], v180 offset:0
	ds_read_b64_tr_b16 v[216:217], v180 offset:4096
	ds_read_b64_tr_b16 v[218:219], v181 offset:0
	ds_read_b64_tr_b16 v[220:221], v181 offset:4096
	ds_read_b64_tr_b16 v[222:223], v180 offset:512
	ds_read_b64_tr_b16 v[224:225], v180 offset:4608
	ds_read_b64_tr_b16 v[226:227], v181 offset:512
	ds_read_b64_tr_b16 v[228:229], v181 offset:4608
	ds_read_b64_tr_b16 v[230:231], v180 offset:1024
	ds_read_b64_tr_b16 v[232:233], v180 offset:5120
	ds_read_b64_tr_b16 v[234:235], v181 offset:1024
	ds_read_b64_tr_b16 v[236:237], v181 offset:5120
	s_waitcnt lgkmcnt(12)
	v_mfma_f32_16x16x32_bf16 v[82:85], v[206:209], v[110:113], v[82:85]
	v_mfma_f32_16x16x32_bf16 v[86:89], v[206:209], v[126:129], v[86:89]
	v_mfma_f32_16x16x32_bf16 v[90:93], v[210:213], v[110:113], v[90:93]
	v_mfma_f32_16x16x32_bf16 v[94:97], v[210:213], v[126:129], v[94:97]
	s_waitcnt vmcnt(0) lgkmcnt(0)
	s_barrier
; #define SBAR() __builtin_amdgcn_sched_barrier(0)
; #define RESC(a) do { if (__any((a) < 1.f)) { if (hi == 0) al_l[r32] = (a); asm volatile("s_waitcnt lgkmcnt(0)" ::: "memory"); \
;     for (int d = 0; d < 4; ++d) for (int r = 0; r < 16; ++r) o[d][r] *= al_l[crow(r, hi)]; } } while (0)
; #define RESC(a) do { if (__any((a) < 1.f)) { if (hi == 0) al_l[r32] = (a); asm volatile("s_waitcnt lgkmcnt(0)" ::: "memory"); \
;     for (int d = 0; d < 4; ++d) for (int r = 0; r < 16; ++r) o[d][r] *= al_l[crow(r, hi)]; } } while (0)
; #define ATT_SYNC(jn) do { ATT_WAIT_BAR(); if ((jn) < NT) ATT_DMA((jn), (jn) & 3); } while (0)
; __device__ __forceinline__ void attn_dma_body(const bf16_t* __restrict__ Qb, int ldq, int tpos0, const float* __restrict__ rope, const float* __restrict__ qgain, ...
;     ...
;   for (int j = 1; j + 1 < NT; j += 2) {
;     { SBAR(); qkt(pB0, pB1, (const bf16_t*)(lds + (j & 3) * SHM_SLOT), qr, r32, hi);
;       finishSM(pA0, pA1, alA, l_reg, pa0, pa1, pa2, pa3); s16x4 va[8]; pv_rd<0>(va, vb0 + ((j - 1) & 3) * (int)SHM_SLOT); SBAR();
;       if (!lead) ATT_SYNC(j + 2);
;       pv_d0_pre(o, vb0 + ((j - 1) & 3) * (int)SHM_SLOT, va, pa0, pa1, pa2, pa3); partialSM(pB0, pB1, m_reg, mnB, alB);
;       if (lead) ATT_SYNC(j + 2);
;       RESC(alB); }
;     { SBAR(); qkt(pA0, pA1, (const bf16_t*)(lds + ((j + 1) & 3) * SHM_SLOT), qr, r32, hi);
;       finishSM(pB0, pB1, alB, l_reg, pa0, pa1, pa2, pa3); s16x4 va[8]; pv_rd<0>(va, vb0 + (j & 3) * (int)SHM_SLOT); SBAR();
;       if (!lead) ATT_SYNC(j + 3);
;       pv_d0_pre(o, vb0 + (j & 3) * (int)SHM_SLOT, va, pa0, pa1, pa2, pa3); partialSM(pA0, pA1, m_reg, mnA, alA);
;       if (lead) ATT_SYNC(j + 3);
;       RESC(alA); }
;   }
	s_cmp_ge_u32 s97, 130
	s_cbranch_scc1 .Lf16_se_N2
	s_add_i32 m0, s96, 0x8000
	s_nop 0
	global_load_lds_dwordx4 v170, s[2:3]
	s_add_i32 m0, s96, 0xa000
	s_nop 0
	global_load_lds_dwordx4 v172, s[2:3]
	s_add_i32 m0, s96, 0xc000
	s_nop 0
	global_load_lds_dwordx4 v171, s[2:3]
	s_add_i32 m0, s96, 0xe000
	s_nop 0
	global_load_lds_dwordx4 v173, s[2:3]
	s_add_u32 s2, s2, 0x4000
	s_addc_u32 s3, s3, 0
.Lf16_se_N2:
	s_waitcnt lgkmcnt(8)
	v_mfma_f32_16x16x32_bf16 v[2:5], v[214:217], v[130:133], v[2:5]
	v_exp_f32_e32 v66, v66
	v_mfma_f32_16x16x32_bf16 v[6:9], v[214:217], v[138:141], v[6:9]
	v_exp_f32_e32 v67, v67
	v_mfma_f32_16x16x32_bf16 v[10:13], v[218:221], v[130:133], v[10:13]
	v_exp_f32_e32 v68, v68
	v_mfma_f32_16x16x32_bf16 v[14:17], v[218:221], v[138:141], v[14:17]
	v_exp_f32_e32 v69, v69
	ds_read_b64_tr_b16 v[238:239], v180 offset:1536
	ds_read_b64_tr_b16 v[240:241], v180 offset:5632
	ds_read_b64_tr_b16 v[242:243], v181 offset:1536
	ds_read_b64_tr_b16 v[244:245], v181 offset:5632
	s_waitcnt lgkmcnt(8)
	v_mfma_f32_16x16x32_bf16 v[18:21], v[222:225], v[130:133], v[18:21]
	v_exp_f32_e32 v70, v70
	v_mfma_f32_16x16x32_bf16 v[22:25], v[222:225], v[138:141], v[22:25]
	v_exp_f32_e32 v71, v71
	v_mfma_f32_16x16x32_bf16 v[26:29], v[226:229], v[130:133], v[26:29]
	v_exp_f32_e32 v72, v72
	v_mfma_f32_16x16x32_bf16 v[30:33], v[226:229], v[138:141], v[30:33]
	v_exp_f32_e32 v73, v73
	v_mfma_f32_16x16x32_bf16 v[246:249], v[194:197], v[130:133], v[246:249]
	ds_read_b64_tr_b16 v[214:215], v180 offset:8192
	ds_read_b64_tr_b16 v[216:217], v180 offset:12288
	ds_read_b64_tr_b16 v[218:219], v181 offset:8192
	ds_read_b64_tr_b16 v[220:221], v181 offset:12288
	s_waitcnt lgkmcnt(8)
	v_mfma_f32_16x16x32_bf16 v[34:37], v[230:233], v[130:133], v[34:37]
	v_exp_f32_e32 v74, v74
	v_mfma_f32_16x16x32_bf16 v[38:41], v[230:233], v[138:141], v[38:41]
	v_exp_f32_e32 v75, v75
	v_mfma_f32_16x16x32_bf16 v[42:45], v[234:237], v[130:133], v[42:45]
	v_exp_f32_e32 v76, v76
	v_mfma_f32_16x16x32_bf16 v[46:49], v[234:237], v[138:141], v[46:49]
	v_exp_f32_e32 v77, v77
	ds_read_b64_tr_b16 v[222:223], v180 offset:8704
	ds_read_b64_tr_b16 v[224:225], v180 offset:12800
	ds_read_b64_tr_b16 v[226:227], v181 offset:8704
	ds_read_b64_tr_b16 v[228:229], v181 offset:12800
	s_waitcnt lgkmcnt(8)
	v_mfma_f32_16x16x32_bf16 v[50:53], v[238:241], v[130:133], v[50:53]
	v_exp_f32_e32 v78, v78
	v_mfma_f32_16x16x32_bf16 v[54:57], v[238:241], v[138:141], v[54:57]
	v_exp_f32_e32 v79, v79
	v_mfma_f32_16x16x32_bf16 v[58:61], v[242:245], v[130:133], v[58:61]
	v_exp_f32_e32 v80, v80
	v_mfma_f32_16x16x32_bf16 v[62:65], v[242:245], v[138:141], v[62:65]
	v_exp_f32_e32 v81, v81
	v_mfma_f32_16x16x32_bf16 v[252:255], v[194:197], v[138:141], v[252:255]
	ds_read_b64_tr_b16 v[230:231], v180 offset:9216
	ds_read_b64_tr_b16 v[232:233], v180 offset:13312
	ds_read_b64_tr_b16 v[234:235], v181 offset:9216
	ds_read_b64_tr_b16 v[236:237], v181 offset:13312
	s_waitcnt lgkmcnt(8)
	v_mfma_f32_16x16x32_bf16 v[2:5], v[214:217], v[134:137], v[2:5]
	v_exp_f32_e32 v82, v82
	v_mfma_f32_16x16x32_bf16 v[6:9], v[214:217], v[142:145], v[6:9]
	v_exp_f32_e32 v83, v83
	v_mfma_f32_16x16x32_bf16 v[10:13], v[218:221], v[134:137], v[10:13]
	v_exp_f32_e32 v84, v84
	v_mfma_f32_16x16x32_bf16 v[14:17], v[218:221], v[142:145], v[14:17]
	v_exp_f32_e32 v85, v85
	ds_read_b64_tr_b16 v[238:239], v180 offset:9728
	ds_read_b64_tr_b16 v[240:241], v180 offset:13824
	ds_read_b64_tr_b16 v[242:243], v181 offset:9728
	ds_read_b64_tr_b16 v[244:245], v181 offset:13824
	s_waitcnt lgkmcnt(8)
	v_mfma_f32_16x16x32_bf16 v[18:21], v[222:225], v[134:137], v[18:21]
	v_exp_f32_e32 v86, v86
	v_mfma_f32_16x16x32_bf16 v[22:25], v[222:225], v[142:145], v[22:25]
	v_exp_f32_e32 v87, v87
	v_mfma_f32_16x16x32_bf16 v[26:29], v[226:229], v[134:137], v[26:29]
	v_exp_f32_e32 v88, v88
	v_mfma_f32_16x16x32_bf16 v[30:33], v[226:229], v[142:145], v[30:33]
	v_exp_f32_e32 v89, v89
	v_mfma_f32_16x16x32_bf16 v[246:249], v[194:197], v[134:137], v[246:249]
	s_waitcnt lgkmcnt(4)
	v_mfma_f32_16x16x32_bf16 v[34:37], v[230:233], v[134:137], v[34:37]
	v_exp_f32_e32 v90, v90
	v_mfma_f32_16x16x32_bf16 v[38:41], v[230:233], v[142:145], v[38:41]
	v_exp_f32_e32 v91, v91
	v_mfma_f32_16x16x32_bf16 v[42:45], v[234:237], v[134:137], v[42:45]
	v_exp_f32_e32 v92, v92
	v_mfma_f32_16x16x32_bf16 v[46:49], v[234:237], v[142:145], v[46:49]
	v_exp_f32_e32 v93, v93
	s_waitcnt lgkmcnt(0)
	v_mfma_f32_16x16x32_bf16 v[50:53], v[238:241], v[134:137], v[50:53]
	v_exp_f32_e32 v94, v94
	v_mfma_f32_16x16x32_bf16 v[54:57], v[238:241], v[142:145], v[54:57]
	v_exp_f32_e32 v95, v95
	v_mfma_f32_16x16x32_bf16 v[58:61], v[242:245], v[134:137], v[58:61]
	v_exp_f32_e32 v96, v96
	v_mfma_f32_16x16x32_bf16 v[62:65], v[242:245], v[142:145], v[62:65]
	v_exp_f32_e32 v97, v97
	v_mfma_f32_16x16x32_bf16 v[252:255], v[194:197], v[142:145], v[252:255]
	v_cvt_pk_bf16_f32 v130, v66, v67
	v_cvt_pk_bf16_f32 v131, v68, v69
	v_cvt_pk_bf16_f32 v132, v74, v75
	v_cvt_pk_bf16_f32 v133, v76, v77
	v_cvt_pk_bf16_f32 v134, v82, v83
	v_cvt_pk_bf16_f32 v135, v84, v85
	v_cvt_pk_bf16_f32 v136, v90, v91
	v_cvt_pk_bf16_f32 v137, v92, v93
	v_cvt_pk_bf16_f32 v138, v70, v71
	v_cvt_pk_bf16_f32 v139, v72, v73
	v_cvt_pk_bf16_f32 v140, v78, v79
	v_cvt_pk_bf16_f32 v141, v80, v81
	v_cvt_pk_bf16_f32 v142, v86, v87
	v_cvt_pk_bf16_f32 v143, v88, v89
	v_cvt_pk_bf16_f32 v144, v94, v95
	v_cvt_pk_bf16_f32 v145, v96, v97
	s_add_i32 s97, s97, 1
	s_cmp_lt_u32 s97, 132
	s_cbranch_scc0 .Lf16_done
; #define SBAR() __builtin_amdgcn_sched_barrier(0)
; #define RESC(a) do { if (__any((a) < 1.f)) { if (hi == 0) al_l[r32] = (a); asm volatile("s_waitcnt lgkmcnt(0)" ::: "memory"); \
;     for (int d = 0; d < 4; ++d) for (int r = 0; r < 16; ++r) o[d][r] *= al_l[crow(r, hi)]; } } while (0)
; #define RESC(a) do { if (__any((a) < 1.f)) { if (hi == 0) al_l[r32] = (a); asm volatile("s_waitcnt lgkmcnt(0)" ::: "memory"); \
;     for (int d = 0; d < 4; ++d) for (int r = 0; r < 16; ++r) o[d][r] *= al_l[crow(r, hi)]; } } while (0)
; #define ATT_SYNC(jn) do { ATT_WAIT_BAR(); if ((jn) < NT) ATT_DMA((jn), (jn) & 3); } while (0)
; __device__ __forceinline__ void attn_dma_body(const bf16_t* __restrict__ Qb, int ldq, int tpos0, const float* __restrict__ rope, const float* __restrict__ qgain, ...
;     ...
;   for (int j = 1; j + 1 < NT; j += 2) {
;     { SBAR(); qkt(pB0, pB1, (const bf16_t*)(lds + (j & 3) * SHM_SLOT), qr, r32, hi);
;       finishSM(pA0, pA1, alA, l_reg, pa0, pa1, pa2, pa3); s16x4 va[8]; pv_rd<0>(va, vb0 + ((j - 1) & 3) * (int)SHM_SLOT); SBAR();
;       if (!lead) ATT_SYNC(j + 2);
;       pv_d0_pre(o, vb0 + ((j - 1) & 3) * (int)SHM_SLOT, va, pa0, pa1, pa2, pa3); partialSM(pB0, pB1, m_reg, mnB, alB);
;       if (lead) ATT_SYNC(j + 2);
;       RESC(alB); }
;     { SBAR(); qkt(pA0, pA1, (const bf16_t*)(lds + ((j + 1) & 3) * SHM_SLOT), qr, r32, hi);
;       finishSM(pB0, pB1, alB, l_reg, pa0, pa1, pa2, pa3); s16x4 va[8]; pv_rd<0>(va, vb0 + (j & 3) * (int)SHM_SLOT); SBAR();
;       if (!lead) ATT_SYNC(j + 3);
;       pv_d0_pre(o, vb0 + (j & 3) * (int)SHM_SLOT, va, pa0, pa1, pa2, pa3); partialSM(pA0, pA1, m_reg, mnA, alA);
;       if (lead) ATT_SYNC(j + 3);
;       RESC(alA); }
;   }
	ds_read_b128 v[146:149], v183 offset:0
	ds_read_b128 v[150:153], v183 offset:4096
	ds_read_b128 v[154:157], v183 offset:8192
	ds_read_b128 v[158:161], v183 offset:12288
	ds_read_b128 v[198:201], v184 offset:0
	ds_read_b128 v[202:205], v184 offset:4096
	ds_read_b128 v[206:209], v184 offset:8192
	ds_read_b128 v[210:213], v184 offset:12288
	s_waitcnt lgkmcnt(6)
	v_mfma_f32_16x16x32_bf16 v[66:69], v[146:149], v[98:101], 0
	v_mfma_f32_16x16x32_bf16 v[70:73], v[146:149], v[114:117], 0
	v_mfma_f32_16x16x32_bf16 v[74:77], v[150:153], v[98:101], 0
	v_mfma_f32_16x16x32_bf16 v[78:81], v[150:153], v[114:117], 0
	ds_read_b128 v[146:149], v185 offset:0
	ds_read_b128 v[150:153], v185 offset:4096
	s_waitcnt lgkmcnt(6)
	v_mfma_f32_16x16x32_bf16 v[82:85], v[154:157], v[98:101], 0
	v_mfma_f32_16x16x32_bf16 v[86:89], v[154:157], v[114:117], 0
	v_mfma_f32_16x16x32_bf16 v[90:93], v[158:161], v[98:101], 0
	v_mfma_f32_16x16x32_bf16 v[94:97], v[158:161], v[114:117], 0
	ds_read_b128 v[154:157], v185 offset:8192
	ds_read_b128 v[158:161], v185 offset:12288
	s_waitcnt lgkmcnt(6)
	v_mfma_f32_16x16x32_bf16 v[66:69], v[198:201], v[102:105], v[66:69]
	v_mfma_f32_16x16x32_bf16 v[70:73], v[198:201], v[118:121], v[70:73]
	v_mfma_f32_16x16x32_bf16 v[74:77], v[202:205], v[102:105], v[74:77]
	v_mfma_f32_16x16x32_bf16 v[78:81], v[202:205], v[118:121], v[78:81]
	ds_read_b128 v[198:201], v186 offset:0
	ds_read_b128 v[202:205], v186 offset:4096
	s_waitcnt lgkmcnt(6)
	v_mfma_f32_16x16x32_bf16 v[82:85], v[206:209], v[102:105], v[82:85]
	v_mfma_f32_16x16x32_bf16 v[86:89], v[206:209], v[118:121], v[86:89]
	v_mfma_f32_16x16x32_bf16 v[90:93], v[210:213], v[102:105], v[90:93]
	v_mfma_f32_16x16x32_bf16 v[94:97], v[210:213], v[118:121], v[94:97]
	ds_read_b128 v[206:209], v186 offset:8192
	ds_read_b128 v[210:213], v186 offset:12288
	s_waitcnt lgkmcnt(6)
	v_mfma_f32_16x16x32_bf16 v[66:69], v[146:149], v[106:109], v[66:69]
	v_mfma_f32_16x16x32_bf16 v[70:73], v[146:149], v[122:125], v[70:73]
	v_mfma_f32_16x16x32_bf16 v[74:77], v[150:153], v[106:109], v[74:77]
	v_mfma_f32_16x16x32_bf16 v[78:81], v[150:153], v[122:125], v[78:81]
	s_waitcnt lgkmcnt(4)
	v_mfma_f32_16x16x32_bf16 v[82:85], v[154:157], v[106:109], v[82:85]
	v_mfma_f32_16x16x32_bf16 v[86:89], v[154:157], v[122:125], v[86:89]
	v_mfma_f32_16x16x32_bf16 v[90:93], v[158:161], v[106:109], v[90:93]
	v_mfma_f32_16x16x32_bf16 v[94:97], v[158:161], v[122:125], v[94:97]
	s_waitcnt lgkmcnt(2)
	v_mfma_f32_16x16x32_bf16 v[66:69], v[198:201], v[110:113], v[66:69]
	v_mfma_f32_16x16x32_bf16 v[70:73], v[198:201], v[126:129], v[70:73]
	v_mfma_f32_16x16x32_bf16 v[74:77], v[202:205], v[110:113], v[74:77]
	v_mfma_f32_16x16x32_bf16 v[78:81], v[202:205], v[126:129], v[78:81]
	ds_read_b64_tr_b16 v[214:215], v180 offset:32768
	ds_read_b64_tr_b16 v[216:217], v180 offset:36864
	ds_read_b64_tr_b16 v[218:219], v181 offset:32768
	ds_read_b64_tr_b16 v[220:221], v181 offset:36864
	ds_read_b64_tr_b16 v[222:223], v180 offset:33280
	ds_read_b64_tr_b16 v[224:225], v180 offset:37376
	ds_read_b64_tr_b16 v[226:227], v181 offset:33280
	ds_read_b64_tr_b16 v[228:229], v181 offset:37376
	ds_read_b64_tr_b16 v[230:231], v180 offset:33792
	ds_read_b64_tr_b16 v[232:233], v180 offset:37888
	ds_read_b64_tr_b16 v[234:235], v181 offset:33792
	ds_read_b64_tr_b16 v[236:237], v181 offset:37888
	s_waitcnt lgkmcnt(12)
	v_mfma_f32_16x16x32_bf16 v[82:85], v[206:209], v[110:113], v[82:85]
	v_mfma_f32_16x16x32_bf16 v[86:89], v[206:209], v[126:129], v[86:89]
	v_mfma_f32_16x16x32_bf16 v[90:93], v[210:213], v[110:113], v[90:93]
	v_mfma_f32_16x16x32_bf16 v[94:97], v[210:213], v[126:129], v[94:97]
	s_waitcnt vmcnt(0) lgkmcnt(0)
	s_barrier
	s_cmp_ge_u32 s97, 130
	s_cbranch_scc1 .Lf16_se_N3
	s_add_i32 m0, s96, 0x10000
	s_nop 0
	global_load_lds_dwordx4 v170, s[2:3]
	s_add_i32 m0, s96, 0x12000
	s_nop 0
	global_load_lds_dwordx4 v172, s[2:3]
	s_add_i32 m0, s96, 0x14000
	s_nop 0
	global_load_lds_dwordx4 v171, s[2:3]
	s_add_i32 m0, s96, 0x16000
	s_nop 0
	global_load_lds_dwordx4 v173, s[2:3]
	s_add_u32 s2, s2, 0x4000
	s_addc_u32 s3, s3, 0
.Lf16_se_N3:
	s_waitcnt lgkmcnt(8)
	v_mfma_f32_16x16x32_bf16 v[2:5], v[214:217], v[130:133], v[2:5]
	v_exp_f32_e32 v66, v66
	v_mfma_f32_16x16x32_bf16 v[6:9], v[214:217], v[138:141], v[6:9]
	v_exp_f32_e32 v67, v67
	v_mfma_f32_16x16x32_bf16 v[10:13], v[218:221], v[130:133], v[10:13]
	v_exp_f32_e32 v68, v68
	v_mfma_f32_16x16x32_bf16 v[14:17], v[218:221], v[138:141], v[14:17]
	v_exp_f32_e32 v69, v69
	ds_read_b64_tr_b16 v[238:239], v180 offset:34304
	ds_read_b64_tr_b16 v[240:241], v180 offset:38400
	ds_read_b64_tr_b16 v[242:243], v181 offset:34304
	ds_read_b64_tr_b16 v[244:245], v181 offset:38400
	s_waitcnt lgkmcnt(8)
	v_mfma_f32_16x16x32_bf16 v[18:21], v[222:225], v[130:133], v[18:21]
	v_exp_f32_e32 v70, v70
	v_mfma_f32_16x16x32_bf16 v[22:25], v[222:225], v[138:141], v[22:25]
	v_exp_f32_e32 v71, v71
	v_mfma_f32_16x16x32_bf16 v[26:29], v[226:229], v[130:133], v[26:29]
	v_exp_f32_e32 v72, v72
	v_mfma_f32_16x16x32_bf16 v[30:33], v[226:229], v[138:141], v[30:33]
	v_exp_f32_e32 v73, v73
	v_mfma_f32_16x16x32_bf16 v[246:249], v[194:197], v[130:133], v[246:249]
	ds_read_b64_tr_b16 v[214:215], v180 offset:40960
	ds_read_b64_tr_b16 v[216:217], v180 offset:45056
	ds_read_b64_tr_b16 v[218:219], v181 offset:40960
	ds_read_b64_tr_b16 v[220:221], v181 offset:45056
	s_waitcnt lgkmcnt(8)
	v_mfma_f32_16x16x32_bf16 v[34:37], v[230:233], v[130:133], v[34:37]
	v_exp_f32_e32 v74, v74
	v_mfma_f32_16x16x32_bf16 v[38:41], v[230:233], v[138:141], v[38:41]
	v_exp_f32_e32 v75, v75
	v_mfma_f32_16x16x32_bf16 v[42:45], v[234:237], v[130:133], v[42:45]
	v_exp_f32_e32 v76, v76
	v_mfma_f32_16x16x32_bf16 v[46:49], v[234:237], v[138:141], v[46:49]
	v_exp_f32_e32 v77, v77
	ds_read_b64_tr_b16 v[222:223], v180 offset:41472
	ds_read_b64_tr_b16 v[224:225], v180 offset:45568
	ds_read_b64_tr_b16 v[226:227], v181 offset:41472
	ds_read_b64_tr_b16 v[228:229], v181 offset:45568
	s_waitcnt lgkmcnt(8)
; #define SBAR() __builtin_amdgcn_sched_barrier(0)
; #define RESC(a) do { if (__any((a) < 1.f)) { if (hi == 0) al_l[r32] = (a); asm volatile("s_waitcnt lgkmcnt(0)" ::: "memory"); \
;     for (int d = 0; d < 4; ++d) for (int r = 0; r < 16; ++r) o[d][r] *= al_l[crow(r, hi)]; } } while (0)
; #define RESC(a) do { if (__any((a) < 1.f)) { if (hi == 0) al_l[r32] = (a); asm volatile("s_waitcnt lgkmcnt(0)" ::: "memory"); \
;     for (int d = 0; d < 4; ++d) for (int r = 0; r < 16; ++r) o[d][r] *= al_l[crow(r, hi)]; } } while (0)
; #define ATT_SYNC(jn) do { ATT_WAIT_BAR(); if ((jn) < NT) ATT_DMA((jn), (jn) & 3); } while (0)
; __device__ __forceinline__ void attn_dma_body(const bf16_t* __restrict__ Qb, int ldq, int tpos0, const float* __restrict__ rope, const float* __restrict__ qgain, ...
;     ...
;   for (int j = 1; j + 1 < NT; j += 2) {
;     { SBAR(); qkt(pB0, pB1, (const bf16_t*)(lds + (j & 3) * SHM_SLOT), qr, r32, hi);
;       finishSM(pA0, pA1, alA, l_reg, pa0, pa1, pa2, pa3); s16x4 va[8]; pv_rd<0>(va, vb0 + ((j - 1) & 3) * (int)SHM_SLOT); SBAR();
;       if (!lead) ATT_SYNC(j + 2);
;       pv_d0_pre(o, vb0 + ((j - 1) & 3) * (int)SHM_SLOT, va, pa0, pa1, pa2, pa3); partialSM(pB0, pB1, m_reg, mnB, alB);
;       if (lead) ATT_SYNC(j + 2);
;       RESC(alB); }
;     { SBAR(); qkt(pA0, pA1, (const bf16_t*)(lds + ((j + 1) & 3) * SHM_SLOT), qr, r32, hi);
;       finishSM(pB0, pB1, alB, l_reg, pa0, pa1, pa2, pa3); s16x4 va[8]; pv_rd<0>(va, vb0 + (j & 3) * (int)SHM_SLOT); SBAR();
;       if (!lead) ATT_SYNC(j + 3);
;       pv_d0_pre(o, vb0 + (j & 3) * (int)SHM_SLOT, va, pa0, pa1, pa2, pa3); partialSM(pA0, pA1, m_reg, mnA, alA);
;       if (lead) ATT_SYNC(j + 3);
;       RESC(alA); }
;   }
	v_mfma_f32_16x16x32_bf16 v[50:53], v[238:241], v[130:133], v[50:53]
	v_exp_f32_e32 v78, v78
	v_mfma_f32_16x16x32_bf16 v[54:57], v[238:241], v[138:141], v[54:57]
	v_exp_f32_e32 v79, v79
	v_mfma_f32_16x16x32_bf16 v[58:61], v[242:245], v[130:133], v[58:61]
	v_exp_f32_e32 v80, v80
	v_mfma_f32_16x16x32_bf16 v[62:65], v[242:245], v[138:141], v[62:65]
	v_exp_f32_e32 v81, v81
	v_mfma_f32_16x16x32_bf16 v[252:255], v[194:197], v[138:141], v[252:255]
	ds_read_b64_tr_b16 v[230:231], v180 offset:41984
	ds_read_b64_tr_b16 v[232:233], v180 offset:46080
	ds_read_b64_tr_b16 v[234:235], v181 offset:41984
	ds_read_b64_tr_b16 v[236:237], v181 offset:46080
	s_waitcnt lgkmcnt(8)
	v_mfma_f32_16x16x32_bf16 v[2:5], v[214:217], v[134:137], v[2:5]
	v_exp_f32_e32 v82, v82
	v_mfma_f32_16x16x32_bf16 v[6:9], v[214:217], v[142:145], v[6:9]
	v_exp_f32_e32 v83, v83
	v_mfma_f32_16x16x32_bf16 v[10:13], v[218:221], v[134:137], v[10:13]
	v_exp_f32_e32 v84, v84
	v_mfma_f32_16x16x32_bf16 v[14:17], v[218:221], v[142:145], v[14:17]
	v_exp_f32_e32 v85, v85
	ds_read_b64_tr_b16 v[238:239], v180 offset:42496
	ds_read_b64_tr_b16 v[240:241], v180 offset:46592
	ds_read_b64_tr_b16 v[242:243], v181 offset:42496
	ds_read_b64_tr_b16 v[244:245], v181 offset:46592
	s_waitcnt lgkmcnt(8)
	v_mfma_f32_16x16x32_bf16 v[18:21], v[222:225], v[134:137], v[18:21]
	v_exp_f32_e32 v86, v86
	v_mfma_f32_16x16x32_bf16 v[22:25], v[222:225], v[142:145], v[22:25]
	v_exp_f32_e32 v87, v87
	v_mfma_f32_16x16x32_bf16 v[26:29], v[226:229], v[134:137], v[26:29]
	v_exp_f32_e32 v88, v88
	v_mfma_f32_16x16x32_bf16 v[30:33], v[226:229], v[142:145], v[30:33]
	v_exp_f32_e32 v89, v89
	v_mfma_f32_16x16x32_bf16 v[246:249], v[194:197], v[134:137], v[246:249]
	s_waitcnt lgkmcnt(4)
	v_mfma_f32_16x16x32_bf16 v[34:37], v[230:233], v[134:137], v[34:37]
	v_exp_f32_e32 v90, v90
	v_mfma_f32_16x16x32_bf16 v[38:41], v[230:233], v[142:145], v[38:41]
	v_exp_f32_e32 v91, v91
	v_mfma_f32_16x16x32_bf16 v[42:45], v[234:237], v[134:137], v[42:45]
	v_exp_f32_e32 v92, v92
	v_mfma_f32_16x16x32_bf16 v[46:49], v[234:237], v[142:145], v[46:49]
	v_exp_f32_e32 v93, v93
	s_waitcnt lgkmcnt(0)
	v_mfma_f32_16x16x32_bf16 v[50:53], v[238:241], v[134:137], v[50:53]
	v_exp_f32_e32 v94, v94
	v_mfma_f32_16x16x32_bf16 v[54:57], v[238:241], v[142:145], v[54:57]
	v_exp_f32_e32 v95, v95
	v_mfma_f32_16x16x32_bf16 v[58:61], v[242:245], v[134:137], v[58:61]
	v_exp_f32_e32 v96, v96
	v_mfma_f32_16x16x32_bf16 v[62:65], v[242:245], v[142:145], v[62:65]
	v_exp_f32_e32 v97, v97
	v_mfma_f32_16x16x32_bf16 v[252:255], v[194:197], v[142:145], v[252:255]
	v_cvt_pk_bf16_f32 v130, v66, v67
	v_cvt_pk_bf16_f32 v131, v68, v69
	v_cvt_pk_bf16_f32 v132, v74, v75
	v_cvt_pk_bf16_f32 v133, v76, v77
	v_cvt_pk_bf16_f32 v134, v82, v83
	v_cvt_pk_bf16_f32 v135, v84, v85
	v_cvt_pk_bf16_f32 v136, v90, v91
	v_cvt_pk_bf16_f32 v137, v92, v93
	v_cvt_pk_bf16_f32 v138, v70, v71
	v_cvt_pk_bf16_f32 v139, v72, v73
	v_cvt_pk_bf16_f32 v140, v78, v79
	v_cvt_pk_bf16_f32 v141, v80, v81
	v_cvt_pk_bf16_f32 v142, v86, v87
	v_cvt_pk_bf16_f32 v143, v88, v89
	v_cvt_pk_bf16_f32 v144, v94, v95
	v_cvt_pk_bf16_f32 v145, v96, v97
	s_add_i32 s97, s97, 1
	s_branch .Lf16_N_loop
	.p2align 6
.Lf16_L_loop:
	ds_read_b128 v[146:149], v183 offset:32768
	ds_read_b128 v[150:153], v183 offset:36864
	ds_read_b128 v[154:157], v183 offset:40960
	ds_read_b128 v[158:161], v183 offset:45056
	ds_read_b128 v[198:201], v184 offset:32768
	ds_read_b128 v[202:205], v184 offset:36864
	ds_read_b128 v[206:209], v184 offset:40960
	ds_read_b128 v[210:213], v184 offset:45056
	s_waitcnt lgkmcnt(6)
	v_mfma_f32_16x16x32_bf16 v[66:69], v[146:149], v[98:101], 0
	v_mfma_f32_16x16x32_bf16 v[70:73], v[146:149], v[114:117], 0
	v_mfma_f32_16x16x32_bf16 v[74:77], v[150:153], v[98:101], 0
	v_mfma_f32_16x16x32_bf16 v[78:81], v[150:153], v[114:117], 0
	ds_read_b128 v[146:149], v185 offset:32768
	ds_read_b128 v[150:153], v185 offset:36864
	s_waitcnt lgkmcnt(6)
	v_mfma_f32_16x16x32_bf16 v[82:85], v[154:157], v[98:101], 0
	v_mfma_f32_16x16x32_bf16 v[86:89], v[154:157], v[114:117], 0
	v_mfma_f32_16x16x32_bf16 v[90:93], v[158:161], v[98:101], 0
	v_mfma_f32_16x16x32_bf16 v[94:97], v[158:161], v[114:117], 0
	ds_read_b128 v[154:157], v185 offset:40960
	ds_read_b128 v[158:161], v185 offset:45056
	s_waitcnt lgkmcnt(6)
	v_mfma_f32_16x16x32_bf16 v[66:69], v[198:201], v[102:105], v[66:69]
	v_mfma_f32_16x16x32_bf16 v[70:73], v[198:201], v[118:121], v[70:73]
	v_mfma_f32_16x16x32_bf16 v[74:77], v[202:205], v[102:105], v[74:77]
	v_mfma_f32_16x16x32_bf16 v[78:81], v[202:205], v[118:121], v[78:81]
	ds_read_b128 v[198:201], v186 offset:32768
	ds_read_b128 v[202:205], v186 offset:36864
	s_waitcnt lgkmcnt(6)
	v_mfma_f32_16x16x32_bf16 v[82:85], v[206:209], v[102:105], v[82:85]
	v_mfma_f32_16x16x32_bf16 v[86:89], v[206:209], v[118:121], v[86:89]
	v_mfma_f32_16x16x32_bf16 v[90:93], v[210:213], v[102:105], v[90:93]
	v_mfma_f32_16x16x32_bf16 v[94:97], v[210:213], v[118:121], v[94:97]
	ds_read_b128 v[206:209], v186 offset:40960
	ds_read_b128 v[210:213], v186 offset:45056
	s_waitcnt lgkmcnt(6)
	v_mfma_f32_16x16x32_bf16 v[66:69], v[146:149], v[106:109], v[66:69]
	v_mfma_f32_16x16x32_bf16 v[70:73], v[146:149], v[122:125], v[70:73]
	v_mfma_f32_16x16x32_bf16 v[74:77], v[150:153], v[106:109], v[74:77]
	v_mfma_f32_16x16x32_bf16 v[78:81], v[150:153], v[122:125], v[78:81]
	s_waitcnt lgkmcnt(4)
	v_mfma_f32_16x16x32_bf16 v[82:85], v[154:157], v[106:109], v[82:85]
	v_mfma_f32_16x16x32_bf16 v[86:89], v[154:157], v[122:125], v[86:89]
	v_mfma_f32_16x16x32_bf16 v[90:93], v[158:161], v[106:109], v[90:93]
	v_mfma_f32_16x16x32_bf16 v[94:97], v[158:161], v[122:125], v[94:97]
	s_waitcnt lgkmcnt(2)
; #define SBAR() __builtin_amdgcn_sched_barrier(0)
; #define RESC(a) do { if (__any((a) < 1.f)) { if (hi == 0) al_l[r32] = (a); asm volatile("s_waitcnt lgkmcnt(0)" ::: "memory"); \
;     for (int d = 0; d < 4; ++d) for (int r = 0; r < 16; ++r) o[d][r] *= al_l[crow(r, hi)]; } } while (0)
; #define RESC(a) do { if (__any((a) < 1.f)) { if (hi == 0) al_l[r32] = (a); asm volatile("s_waitcnt lgkmcnt(0)" ::: "memory"); \
;     for (int d = 0; d < 4; ++d) for (int r = 0; r < 16; ++r) o[d][r] *= al_l[crow(r, hi)]; } } while (0)
; #define ATT_SYNC(jn) do { ATT_WAIT_BAR(); if ((jn) < NT) ATT_DMA((jn), (jn) & 3); } while (0)
; __device__ __forceinline__ void attn_dma_body(const bf16_t* __restrict__ Qb, int ldq, int tpos0, const float* __restrict__ rope, const float* __restrict__ qgain, ...
;     ...
;   for (int j = 1; j + 1 < NT; j += 2) {
;     { SBAR(); qkt(pB0, pB1, (const bf16_t*)(lds + (j & 3) * SHM_SLOT), qr, r32, hi);
;       finishSM(pA0, pA1, alA, l_reg, pa0, pa1, pa2, pa3); s16x4 va[8]; pv_rd<0>(va, vb0 + ((j - 1) & 3) * (int)SHM_SLOT); SBAR();
;       if (!lead) ATT_SYNC(j + 2);
;       pv_d0_pre(o, vb0 + ((j - 1) & 3) * (int)SHM_SLOT, va, pa0, pa1, pa2, pa3); partialSM(pB0, pB1, m_reg, mnB, alB);
;       if (lead) ATT_SYNC(j + 2);
;       RESC(alB); }
;     { SBAR(); qkt(pA0, pA1, (const bf16_t*)(lds + ((j + 1) & 3) * SHM_SLOT), qr, r32, hi);
;       finishSM(pB0, pB1, alB, l_reg, pa0, pa1, pa2, pa3); s16x4 va[8]; pv_rd<0>(va, vb0 + (j & 3) * (int)SHM_SLOT); SBAR();
;       if (!lead) ATT_SYNC(j + 3);
;       pv_d0_pre(o, vb0 + (j & 3) * (int)SHM_SLOT, va, pa0, pa1, pa2, pa3); partialSM(pA0, pA1, m_reg, mnA, alA);
;       if (lead) ATT_SYNC(j + 3);
;       RESC(alA); }
;   }
	v_mfma_f32_16x16x32_bf16 v[66:69], v[198:201], v[110:113], v[66:69]
	v_mfma_f32_16x16x32_bf16 v[70:73], v[198:201], v[126:129], v[70:73]
	v_mfma_f32_16x16x32_bf16 v[74:77], v[202:205], v[110:113], v[74:77]
	v_mfma_f32_16x16x32_bf16 v[78:81], v[202:205], v[126:129], v[78:81]
	ds_read_b64_tr_b16 v[214:215], v191 offset:0
	ds_read_b64_tr_b16 v[216:217], v191 offset:4096
	ds_read_b64_tr_b16 v[218:219], v192 offset:0
	ds_read_b64_tr_b16 v[220:221], v192 offset:4096
	ds_read_b64_tr_b16 v[222:223], v191 offset:512
	ds_read_b64_tr_b16 v[224:225], v191 offset:4608
	ds_read_b64_tr_b16 v[226:227], v192 offset:512
	ds_read_b64_tr_b16 v[228:229], v192 offset:4608
	ds_read_b64_tr_b16 v[230:231], v191 offset:1024
	ds_read_b64_tr_b16 v[232:233], v191 offset:5120
	ds_read_b64_tr_b16 v[234:235], v192 offset:1024
	ds_read_b64_tr_b16 v[236:237], v192 offset:5120
	s_waitcnt lgkmcnt(12)
	v_mfma_f32_16x16x32_bf16 v[82:85], v[206:209], v[110:113], v[82:85]
	v_mfma_f32_16x16x32_bf16 v[86:89], v[206:209], v[126:129], v[86:89]
	v_mfma_f32_16x16x32_bf16 v[90:93], v[210:213], v[110:113], v[90:93]
	v_mfma_f32_16x16x32_bf16 v[94:97], v[210:213], v[126:129], v[94:97]
	s_waitcnt lgkmcnt(8)
	v_mfma_f32_16x16x32_bf16 v[2:5], v[214:217], v[130:133], v[2:5]
	v_exp_f32_e32 v66, v66
	v_mfma_f32_16x16x32_bf16 v[6:9], v[214:217], v[138:141], v[6:9]
	v_exp_f32_e32 v67, v67
	v_mfma_f32_16x16x32_bf16 v[10:13], v[218:221], v[130:133], v[10:13]
	v_exp_f32_e32 v68, v68
	v_mfma_f32_16x16x32_bf16 v[14:17], v[218:221], v[138:141], v[14:17]
	v_exp_f32_e32 v69, v69
	ds_read_b64_tr_b16 v[238:239], v191 offset:1536
	ds_read_b64_tr_b16 v[240:241], v191 offset:5632
	ds_read_b64_tr_b16 v[242:243], v192 offset:1536
	ds_read_b64_tr_b16 v[244:245], v192 offset:5632
	s_waitcnt lgkmcnt(8)
	v_mfma_f32_16x16x32_bf16 v[18:21], v[222:225], v[130:133], v[18:21]
	v_exp_f32_e32 v70, v70
	v_mfma_f32_16x16x32_bf16 v[22:25], v[222:225], v[138:141], v[22:25]
	v_exp_f32_e32 v71, v71
	v_mfma_f32_16x16x32_bf16 v[26:29], v[226:229], v[130:133], v[26:29]
	v_exp_f32_e32 v72, v72
	v_mfma_f32_16x16x32_bf16 v[30:33], v[226:229], v[138:141], v[30:33]
	v_exp_f32_e32 v73, v73
	v_mfma_f32_16x16x32_bf16 v[246:249], v[194:197], v[130:133], v[246:249]
	ds_read_b64_tr_b16 v[214:215], v191 offset:8192
	ds_read_b64_tr_b16 v[216:217], v191 offset:12288
	ds_read_b64_tr_b16 v[218:219], v192 offset:8192
	ds_read_b64_tr_b16 v[220:221], v192 offset:12288
	s_waitcnt lgkmcnt(8)
	v_mfma_f32_16x16x32_bf16 v[34:37], v[230:233], v[130:133], v[34:37]
	v_exp_f32_e32 v74, v74
	v_mfma_f32_16x16x32_bf16 v[38:41], v[230:233], v[138:141], v[38:41]
	v_exp_f32_e32 v75, v75
	v_mfma_f32_16x16x32_bf16 v[42:45], v[234:237], v[130:133], v[42:45]
	v_exp_f32_e32 v76, v76
	v_mfma_f32_16x16x32_bf16 v[46:49], v[234:237], v[138:141], v[46:49]
	v_exp_f32_e32 v77, v77
	ds_read_b64_tr_b16 v[222:223], v191 offset:8704
	ds_read_b64_tr_b16 v[224:225], v191 offset:12800
	ds_read_b64_tr_b16 v[226:227], v192 offset:8704
	ds_read_b64_tr_b16 v[228:229], v192 offset:12800
	s_waitcnt lgkmcnt(8)
	v_mfma_f32_16x16x32_bf16 v[50:53], v[238:241], v[130:133], v[50:53]
	v_exp_f32_e32 v78, v78
	v_mfma_f32_16x16x32_bf16 v[54:57], v[238:241], v[138:141], v[54:57]
	v_exp_f32_e32 v79, v79
	v_mfma_f32_16x16x32_bf16 v[58:61], v[242:245], v[130:133], v[58:61]
	v_exp_f32_e32 v80, v80
	v_mfma_f32_16x16x32_bf16 v[62:65], v[242:245], v[138:141], v[62:65]
	v_exp_f32_e32 v81, v81
	v_mfma_f32_16x16x32_bf16 v[252:255], v[194:197], v[138:141], v[252:255]
	ds_read_b64_tr_b16 v[230:231], v191 offset:9216
	ds_read_b64_tr_b16 v[232:233], v191 offset:13312
	ds_read_b64_tr_b16 v[234:235], v192 offset:9216
	ds_read_b64_tr_b16 v[236:237], v192 offset:13312
	s_waitcnt lgkmcnt(8)
	v_mfma_f32_16x16x32_bf16 v[2:5], v[214:217], v[134:137], v[2:5]
	v_exp_f32_e32 v82, v82
	v_mfma_f32_16x16x32_bf16 v[6:9], v[214:217], v[142:145], v[6:9]
	v_exp_f32_e32 v83, v83
	v_mfma_f32_16x16x32_bf16 v[10:13], v[218:221], v[134:137], v[10:13]
	v_exp_f32_e32 v84, v84
	v_mfma_f32_16x16x32_bf16 v[14:17], v[218:221], v[142:145], v[14:17]
	v_exp_f32_e32 v85, v85
	ds_read_b64_tr_b16 v[238:239], v191 offset:9728
	ds_read_b64_tr_b16 v[240:241], v191 offset:13824
	ds_read_b64_tr_b16 v[242:243], v192 offset:9728
	ds_read_b64_tr_b16 v[244:245], v192 offset:13824
	s_waitcnt lgkmcnt(8)
	v_mfma_f32_16x16x32_bf16 v[18:21], v[222:225], v[134:137], v[18:21]
	v_exp_f32_e32 v86, v86
	v_mfma_f32_16x16x32_bf16 v[22:25], v[222:225], v[142:145], v[22:25]
	v_exp_f32_e32 v87, v87
	v_mfma_f32_16x16x32_bf16 v[26:29], v[226:229], v[134:137], v[26:29]
	v_exp_f32_e32 v88, v88
	v_mfma_f32_16x16x32_bf16 v[30:33], v[226:229], v[142:145], v[30:33]
	v_exp_f32_e32 v89, v89
	v_mfma_f32_16x16x32_bf16 v[246:249], v[194:197], v[134:137], v[246:249]
	s_waitcnt lgkmcnt(4)
	v_mfma_f32_16x16x32_bf16 v[34:37], v[230:233], v[134:137], v[34:37]
	v_exp_f32_e32 v90, v90
	v_mfma_f32_16x16x32_bf16 v[38:41], v[230:233], v[142:145], v[38:41]
	v_exp_f32_e32 v91, v91
	v_mfma_f32_16x16x32_bf16 v[42:45], v[234:237], v[134:137], v[42:45]
	v_exp_f32_e32 v92, v92
	v_mfma_f32_16x16x32_bf16 v[46:49], v[234:237], v[142:145], v[46:49]
	v_exp_f32_e32 v93, v93
	s_waitcnt lgkmcnt(0)
	v_mfma_f32_16x16x32_bf16 v[50:53], v[238:241], v[134:137], v[50:53]
	v_exp_f32_e32 v94, v94
	v_mfma_f32_16x16x32_bf16 v[54:57], v[238:241], v[142:145], v[54:57]
	v_exp_f32_e32 v95, v95
	v_mfma_f32_16x16x32_bf16 v[58:61], v[242:245], v[134:137], v[58:61]
	v_exp_f32_e32 v96, v96
	v_mfma_f32_16x16x32_bf16 v[62:65], v[242:245], v[142:145], v[62:65]
	v_exp_f32_e32 v97, v97
	v_mfma_f32_16x16x32_bf16 v[252:255], v[194:197], v[142:145], v[252:255]
	s_waitcnt vmcnt(0) lgkmcnt(0)
	s_barrier
	s_cmp_ge_u32 s97, 130
	s_cbranch_scc1 .Lf16_se_L0
	s_add_i32 m0, s96, 0x18000
	s_nop 0
	global_load_lds_dwordx4 v170, s[2:3]
	s_add_i32 m0, s96, 0x1a000
	s_nop 0
	global_load_lds_dwordx4 v172, s[2:3]
	s_add_i32 m0, s96, 0x1c000
	s_nop 0
	global_load_lds_dwordx4 v171, s[2:3]
	s_add_i32 m0, s96, 0x1e000
	s_nop 0
	global_load_lds_dwordx4 v173, s[2:3]
	s_add_u32 s2, s2, 0x4000
	s_addc_u32 s3, s3, 0
; #define SBAR() __builtin_amdgcn_sched_barrier(0)
; #define RESC(a) do { if (__any((a) < 1.f)) { if (hi == 0) al_l[r32] = (a); asm volatile("s_waitcnt lgkmcnt(0)" ::: "memory"); \
;     for (int d = 0; d < 4; ++d) for (int r = 0; r < 16; ++r) o[d][r] *= al_l[crow(r, hi)]; } } while (0)
; #define RESC(a) do { if (__any((a) < 1.f)) { if (hi == 0) al_l[r32] = (a); asm volatile("s_waitcnt lgkmcnt(0)" ::: "memory"); \
;     for (int d = 0; d < 4; ++d) for (int r = 0; r < 16; ++r) o[d][r] *= al_l[crow(r, hi)]; } } while (0)
; #define ATT_SYNC(jn) do { ATT_WAIT_BAR(); if ((jn) < NT) ATT_DMA((jn), (jn) & 3); } while (0)
; __device__ __forceinline__ void attn_dma_body(const bf16_t* __restrict__ Qb, int ldq, int tpos0, const float* __restrict__ rope, const float* __restrict__ qgain, ...
;     ...
;   for (int j = 1; j + 1 < NT; j += 2) {
;     { SBAR(); qkt(pB0, pB1, (const bf16_t*)(lds + (j & 3) * SHM_SLOT), qr, r32, hi);
;       finishSM(pA0, pA1, alA, l_reg, pa0, pa1, pa2, pa3); s16x4 va[8]; pv_rd<0>(va, vb0 + ((j - 1) & 3) * (int)SHM_SLOT); SBAR();
;       if (!lead) ATT_SYNC(j + 2);
;       pv_d0_pre(o, vb0 + ((j - 1) & 3) * (int)SHM_SLOT, va, pa0, pa1, pa2, pa3); partialSM(pB0, pB1, m_reg, mnB, alB);
;       if (lead) ATT_SYNC(j + 2);
;       RESC(alB); }
;     { SBAR(); qkt(pA0, pA1, (const bf16_t*)(lds + ((j + 1) & 3) * SHM_SLOT), qr, r32, hi);
;       finishSM(pB0, pB1, alB, l_reg, pa0, pa1, pa2, pa3); s16x4 va[8]; pv_rd<0>(va, vb0 + (j & 3) * (int)SHM_SLOT); SBAR();
;       if (!lead) ATT_SYNC(j + 3);
;       pv_d0_pre(o, vb0 + (j & 3) * (int)SHM_SLOT, va, pa0, pa1, pa2, pa3); partialSM(pA0, pA1, m_reg, mnA, alA);
;       if (lead) ATT_SYNC(j + 3);
;       RESC(alA); }
;   }
.Lf16_se_L0:
	v_cvt_pk_bf16_f32 v130, v66, v67
	v_cvt_pk_bf16_f32 v131, v68, v69
	v_cvt_pk_bf16_f32 v132, v74, v75
	v_cvt_pk_bf16_f32 v133, v76, v77
	v_cvt_pk_bf16_f32 v134, v82, v83
	v_cvt_pk_bf16_f32 v135, v84, v85
	v_cvt_pk_bf16_f32 v136, v90, v91
	v_cvt_pk_bf16_f32 v137, v92, v93
	v_cvt_pk_bf16_f32 v138, v70, v71
	v_cvt_pk_bf16_f32 v139, v72, v73
	v_cvt_pk_bf16_f32 v140, v78, v79
	v_cvt_pk_bf16_f32 v141, v80, v81
	v_cvt_pk_bf16_f32 v142, v86, v87
	v_cvt_pk_bf16_f32 v143, v88, v89
	v_cvt_pk_bf16_f32 v144, v94, v95
	v_cvt_pk_bf16_f32 v145, v96, v97
	s_add_i32 s97, s97, 1
	ds_read_b128 v[146:149], v187 offset:0
	ds_read_b128 v[150:153], v187 offset:4096
	ds_read_b128 v[154:157], v187 offset:8192
	ds_read_b128 v[158:161], v187 offset:12288
	ds_read_b128 v[198:201], v188 offset:0
	ds_read_b128 v[202:205], v188 offset:4096
	ds_read_b128 v[206:209], v188 offset:8192
	ds_read_b128 v[210:213], v188 offset:12288
	s_waitcnt lgkmcnt(6)
	v_mfma_f32_16x16x32_bf16 v[66:69], v[146:149], v[98:101], 0
	v_mfma_f32_16x16x32_bf16 v[70:73], v[146:149], v[114:117], 0
	v_mfma_f32_16x16x32_bf16 v[74:77], v[150:153], v[98:101], 0
	v_mfma_f32_16x16x32_bf16 v[78:81], v[150:153], v[114:117], 0
	ds_read_b128 v[146:149], v189 offset:0
	ds_read_b128 v[150:153], v189 offset:4096
	s_waitcnt lgkmcnt(6)
	v_mfma_f32_16x16x32_bf16 v[82:85], v[154:157], v[98:101], 0
	v_mfma_f32_16x16x32_bf16 v[86:89], v[154:157], v[114:117], 0
	v_mfma_f32_16x16x32_bf16 v[90:93], v[158:161], v[98:101], 0
	v_mfma_f32_16x16x32_bf16 v[94:97], v[158:161], v[114:117], 0
	ds_read_b128 v[154:157], v189 offset:8192
	ds_read_b128 v[158:161], v189 offset:12288
	s_waitcnt lgkmcnt(6)
	v_mfma_f32_16x16x32_bf16 v[66:69], v[198:201], v[102:105], v[66:69]
	v_mfma_f32_16x16x32_bf16 v[70:73], v[198:201], v[118:121], v[70:73]
	v_mfma_f32_16x16x32_bf16 v[74:77], v[202:205], v[102:105], v[74:77]
	v_mfma_f32_16x16x32_bf16 v[78:81], v[202:205], v[118:121], v[78:81]
	ds_read_b128 v[198:201], v190 offset:0
	ds_read_b128 v[202:205], v190 offset:4096
	s_waitcnt lgkmcnt(6)
	v_mfma_f32_16x16x32_bf16 v[82:85], v[206:209], v[102:105], v[82:85]
	v_mfma_f32_16x16x32_bf16 v[86:89], v[206:209], v[118:121], v[86:89]
	v_mfma_f32_16x16x32_bf16 v[90:93], v[210:213], v[102:105], v[90:93]
	v_mfma_f32_16x16x32_bf16 v[94:97], v[210:213], v[118:121], v[94:97]
	ds_read_b128 v[206:209], v190 offset:8192
	ds_read_b128 v[210:213], v190 offset:12288
	s_waitcnt lgkmcnt(6)
	v_mfma_f32_16x16x32_bf16 v[66:69], v[146:149], v[106:109], v[66:69]
	v_mfma_f32_16x16x32_bf16 v[70:73], v[146:149], v[122:125], v[70:73]
	v_mfma_f32_16x16x32_bf16 v[74:77], v[150:153], v[106:109], v[74:77]
	v_mfma_f32_16x16x32_bf16 v[78:81], v[150:153], v[122:125], v[78:81]
	s_waitcnt lgkmcnt(4)
	v_mfma_f32_16x16x32_bf16 v[82:85], v[154:157], v[106:109], v[82:85]
	v_mfma_f32_16x16x32_bf16 v[86:89], v[154:157], v[122:125], v[86:89]
	v_mfma_f32_16x16x32_bf16 v[90:93], v[158:161], v[106:109], v[90:93]
	v_mfma_f32_16x16x32_bf16 v[94:97], v[158:161], v[122:125], v[94:97]
	s_waitcnt lgkmcnt(2)
	v_mfma_f32_16x16x32_bf16 v[66:69], v[198:201], v[110:113], v[66:69]
	v_mfma_f32_16x16x32_bf16 v[70:73], v[198:201], v[126:129], v[70:73]
	v_mfma_f32_16x16x32_bf16 v[74:77], v[202:205], v[110:113], v[74:77]
	v_mfma_f32_16x16x32_bf16 v[78:81], v[202:205], v[126:129], v[78:81]
	ds_read_b64_tr_b16 v[214:215], v191 offset:32768
	ds_read_b64_tr_b16 v[216:217], v191 offset:36864
	ds_read_b64_tr_b16 v[218:219], v192 offset:32768
	ds_read_b64_tr_b16 v[220:221], v192 offset:36864
	ds_read_b64_tr_b16 v[222:223], v191 offset:33280
	ds_read_b64_tr_b16 v[224:225], v191 offset:37376
	ds_read_b64_tr_b16 v[226:227], v192 offset:33280
	ds_read_b64_tr_b16 v[228:229], v192 offset:37376
	ds_read_b64_tr_b16 v[230:231], v191 offset:33792
	ds_read_b64_tr_b16 v[232:233], v191 offset:37888
	ds_read_b64_tr_b16 v[234:235], v192 offset:33792
	ds_read_b64_tr_b16 v[236:237], v192 offset:37888
	s_waitcnt lgkmcnt(12)
	v_mfma_f32_16x16x32_bf16 v[82:85], v[206:209], v[110:113], v[82:85]
	v_mfma_f32_16x16x32_bf16 v[86:89], v[206:209], v[126:129], v[86:89]
	v_mfma_f32_16x16x32_bf16 v[90:93], v[210:213], v[110:113], v[90:93]
	v_mfma_f32_16x16x32_bf16 v[94:97], v[210:213], v[126:129], v[94:97]
	s_waitcnt lgkmcnt(8)
	v_mfma_f32_16x16x32_bf16 v[2:5], v[214:217], v[130:133], v[2:5]
	v_exp_f32_e32 v66, v66
	v_mfma_f32_16x16x32_bf16 v[6:9], v[214:217], v[138:141], v[6:9]
	v_exp_f32_e32 v67, v67
	v_mfma_f32_16x16x32_bf16 v[10:13], v[218:221], v[130:133], v[10:13]
	v_exp_f32_e32 v68, v68
	v_mfma_f32_16x16x32_bf16 v[14:17], v[218:221], v[138:141], v[14:17]
	v_exp_f32_e32 v69, v69
	ds_read_b64_tr_b16 v[238:239], v191 offset:34304
	ds_read_b64_tr_b16 v[240:241], v191 offset:38400
	ds_read_b64_tr_b16 v[242:243], v192 offset:34304
	ds_read_b64_tr_b16 v[244:245], v192 offset:38400
	s_waitcnt lgkmcnt(8)
	v_mfma_f32_16x16x32_bf16 v[18:21], v[222:225], v[130:133], v[18:21]
	v_exp_f32_e32 v70, v70
	v_mfma_f32_16x16x32_bf16 v[22:25], v[222:225], v[138:141], v[22:25]
	v_exp_f32_e32 v71, v71
	v_mfma_f32_16x16x32_bf16 v[26:29], v[226:229], v[130:133], v[26:29]
	v_exp_f32_e32 v72, v72
	v_mfma_f32_16x16x32_bf16 v[30:33], v[226:229], v[138:141], v[30:33]
	v_exp_f32_e32 v73, v73
	v_mfma_f32_16x16x32_bf16 v[246:249], v[194:197], v[130:133], v[246:249]
	ds_read_b64_tr_b16 v[214:215], v191 offset:40960
	ds_read_b64_tr_b16 v[216:217], v191 offset:45056
	ds_read_b64_tr_b16 v[218:219], v192 offset:40960
	ds_read_b64_tr_b16 v[220:221], v192 offset:45056
	s_waitcnt lgkmcnt(8)
; #define SBAR() __builtin_amdgcn_sched_barrier(0)
; #define RESC(a) do { if (__any((a) < 1.f)) { if (hi == 0) al_l[r32] = (a); asm volatile("s_waitcnt lgkmcnt(0)" ::: "memory"); \
;     for (int d = 0; d < 4; ++d) for (int r = 0; r < 16; ++r) o[d][r] *= al_l[crow(r, hi)]; } } while (0)
; #define RESC(a) do { if (__any((a) < 1.f)) { if (hi == 0) al_l[r32] = (a); asm volatile("s_waitcnt lgkmcnt(0)" ::: "memory"); \
;     for (int d = 0; d < 4; ++d) for (int r = 0; r < 16; ++r) o[d][r] *= al_l[crow(r, hi)]; } } while (0)
; #define ATT_SYNC(jn) do { ATT_WAIT_BAR(); if ((jn) < NT) ATT_DMA((jn), (jn) & 3); } while (0)
; __device__ __forceinline__ void attn_dma_body(const bf16_t* __restrict__ Qb, int ldq, int tpos0, const float* __restrict__ rope, const float* __restrict__ qgain, ...
;     ...
;   for (int j = 1; j + 1 < NT; j += 2) {
;     { SBAR(); qkt(pB0, pB1, (const bf16_t*)(lds + (j & 3) * SHM_SLOT), qr, r32, hi);
;       finishSM(pA0, pA1, alA, l_reg, pa0, pa1, pa2, pa3); s16x4 va[8]; pv_rd<0>(va, vb0 + ((j - 1) & 3) * (int)SHM_SLOT); SBAR();
;       if (!lead) ATT_SYNC(j + 2);
;       pv_d0_pre(o, vb0 + ((j - 1) & 3) * (int)SHM_SLOT, va, pa0, pa1, pa2, pa3); partialSM(pB0, pB1, m_reg, mnB, alB);
;       if (lead) ATT_SYNC(j + 2);
;       RESC(alB); }
;     { SBAR(); qkt(pA0, pA1, (const bf16_t*)(lds + ((j + 1) & 3) * SHM_SLOT), qr, r32, hi);
;       finishSM(pB0, pB1, alB, l_reg, pa0, pa1, pa2, pa3); s16x4 va[8]; pv_rd<0>(va, vb0 + (j & 3) * (int)SHM_SLOT); SBAR();
;       if (!lead) ATT_SYNC(j + 3);
;       pv_d0_pre(o, vb0 + (j & 3) * (int)SHM_SLOT, va, pa0, pa1, pa2, pa3); partialSM(pA0, pA1, m_reg, mnA, alA);
;       if (lead) ATT_SYNC(j + 3);
;       RESC(alA); }
;   }
	v_mfma_f32_16x16x32_bf16 v[34:37], v[230:233], v[130:133], v[34:37]
	v_exp_f32_e32 v74, v74
	v_mfma_f32_16x16x32_bf16 v[38:41], v[230:233], v[138:141], v[38:41]
	v_exp_f32_e32 v75, v75
	v_mfma_f32_16x16x32_bf16 v[42:45], v[234:237], v[130:133], v[42:45]
	v_exp_f32_e32 v76, v76
	v_mfma_f32_16x16x32_bf16 v[46:49], v[234:237], v[138:141], v[46:49]
	v_exp_f32_e32 v77, v77
	ds_read_b64_tr_b16 v[222:223], v191 offset:41472
	ds_read_b64_tr_b16 v[224:225], v191 offset:45568
	ds_read_b64_tr_b16 v[226:227], v192 offset:41472
	ds_read_b64_tr_b16 v[228:229], v192 offset:45568
	s_waitcnt lgkmcnt(8)
	v_mfma_f32_16x16x32_bf16 v[50:53], v[238:241], v[130:133], v[50:53]
	v_exp_f32_e32 v78, v78
	v_mfma_f32_16x16x32_bf16 v[54:57], v[238:241], v[138:141], v[54:57]
	v_exp_f32_e32 v79, v79
	v_mfma_f32_16x16x32_bf16 v[58:61], v[242:245], v[130:133], v[58:61]
	v_exp_f32_e32 v80, v80
	v_mfma_f32_16x16x32_bf16 v[62:65], v[242:245], v[138:141], v[62:65]
	v_exp_f32_e32 v81, v81
	v_mfma_f32_16x16x32_bf16 v[252:255], v[194:197], v[138:141], v[252:255]
	ds_read_b64_tr_b16 v[230:231], v191 offset:41984
	ds_read_b64_tr_b16 v[232:233], v191 offset:46080
	ds_read_b64_tr_b16 v[234:235], v192 offset:41984
	ds_read_b64_tr_b16 v[236:237], v192 offset:46080
	s_waitcnt lgkmcnt(8)
	v_mfma_f32_16x16x32_bf16 v[2:5], v[214:217], v[134:137], v[2:5]
	v_exp_f32_e32 v82, v82
	v_mfma_f32_16x16x32_bf16 v[6:9], v[214:217], v[142:145], v[6:9]
	v_exp_f32_e32 v83, v83
	v_mfma_f32_16x16x32_bf16 v[10:13], v[218:221], v[134:137], v[10:13]
	v_exp_f32_e32 v84, v84
	v_mfma_f32_16x16x32_bf16 v[14:17], v[218:221], v[142:145], v[14:17]
	v_exp_f32_e32 v85, v85
	ds_read_b64_tr_b16 v[238:239], v191 offset:42496
	ds_read_b64_tr_b16 v[240:241], v191 offset:46592
	ds_read_b64_tr_b16 v[242:243], v192 offset:42496
	ds_read_b64_tr_b16 v[244:245], v192 offset:46592
	s_waitcnt lgkmcnt(8)
	v_mfma_f32_16x16x32_bf16 v[18:21], v[222:225], v[134:137], v[18:21]
	v_exp_f32_e32 v86, v86
	v_mfma_f32_16x16x32_bf16 v[22:25], v[222:225], v[142:145], v[22:25]
	v_exp_f32_e32 v87, v87
	v_mfma_f32_16x16x32_bf16 v[26:29], v[226:229], v[134:137], v[26:29]
	v_exp_f32_e32 v88, v88
	v_mfma_f32_16x16x32_bf16 v[30:33], v[226:229], v[142:145], v[30:33]
	v_exp_f32_e32 v89, v89
	v_mfma_f32_16x16x32_bf16 v[246:249], v[194:197], v[134:137], v[246:249]
	s_waitcnt lgkmcnt(4)
	v_mfma_f32_16x16x32_bf16 v[34:37], v[230:233], v[134:137], v[34:37]
	v_exp_f32_e32 v90, v90
	v_mfma_f32_16x16x32_bf16 v[38:41], v[230:233], v[142:145], v[38:41]
	v_exp_f32_e32 v91, v91
	v_mfma_f32_16x16x32_bf16 v[42:45], v[234:237], v[134:137], v[42:45]
	v_exp_f32_e32 v92, v92
	v_mfma_f32_16x16x32_bf16 v[46:49], v[234:237], v[142:145], v[46:49]
	v_exp_f32_e32 v93, v93
	s_waitcnt lgkmcnt(0)
	v_mfma_f32_16x16x32_bf16 v[50:53], v[238:241], v[134:137], v[50:53]
	v_exp_f32_e32 v94, v94
	v_mfma_f32_16x16x32_bf16 v[54:57], v[238:241], v[142:145], v[54:57]
	v_exp_f32_e32 v95, v95
	v_mfma_f32_16x16x32_bf16 v[58:61], v[242:245], v[134:137], v[58:61]
	v_exp_f32_e32 v96, v96
	v_mfma_f32_16x16x32_bf16 v[62:65], v[242:245], v[142:145], v[62:65]
	v_exp_f32_e32 v97, v97
	v_mfma_f32_16x16x32_bf16 v[252:255], v[194:197], v[142:145], v[252:255]
	s_waitcnt vmcnt(0) lgkmcnt(0)
	s_barrier
	s_cmp_ge_u32 s97, 130
	s_cbranch_scc1 .Lf16_se_L1
	s_add_i32 m0, s96, 0x0
	s_nop 0
	global_load_lds_dwordx4 v170, s[2:3]
	s_add_i32 m0, s96, 0x2000
	s_nop 0
	global_load_lds_dwordx4 v172, s[2:3]
	s_add_i32 m0, s96, 0x4000
	s_nop 0
	global_load_lds_dwordx4 v171, s[2:3]
	s_add_i32 m0, s96, 0x6000
	s_nop 0
	global_load_lds_dwordx4 v173, s[2:3]
	s_add_u32 s2, s2, 0x4000
	s_addc_u32 s3, s3, 0
.Lf16_se_L1:
	v_cvt_pk_bf16_f32 v130, v66, v67
	v_cvt_pk_bf16_f32 v131, v68, v69
	v_cvt_pk_bf16_f32 v132, v74, v75
	v_cvt_pk_bf16_f32 v133, v76, v77
	v_cvt_pk_bf16_f32 v134, v82, v83
	v_cvt_pk_bf16_f32 v135, v84, v85
	v_cvt_pk_bf16_f32 v136, v90, v91
	v_cvt_pk_bf16_f32 v137, v92, v93
	v_cvt_pk_bf16_f32 v138, v70, v71
	v_cvt_pk_bf16_f32 v139, v72, v73
	v_cvt_pk_bf16_f32 v140, v78, v79
	v_cvt_pk_bf16_f32 v141, v80, v81
	v_cvt_pk_bf16_f32 v142, v86, v87
	v_cvt_pk_bf16_f32 v143, v88, v89
	v_cvt_pk_bf16_f32 v144, v94, v95
	v_cvt_pk_bf16_f32 v145, v96, v97
	s_add_i32 s97, s97, 1
	ds_read_b128 v[146:149], v187 offset:32768
	ds_read_b128 v[150:153], v187 offset:36864
	ds_read_b128 v[154:157], v187 offset:40960
	ds_read_b128 v[158:161], v187 offset:45056
	ds_read_b128 v[198:201], v188 offset:32768
	ds_read_b128 v[202:205], v188 offset:36864
	ds_read_b128 v[206:209], v188 offset:40960
	ds_read_b128 v[210:213], v188 offset:45056
	s_waitcnt lgkmcnt(6)
	v_mfma_f32_16x16x32_bf16 v[66:69], v[146:149], v[98:101], 0
	v_mfma_f32_16x16x32_bf16 v[70:73], v[146:149], v[114:117], 0
	v_mfma_f32_16x16x32_bf16 v[74:77], v[150:153], v[98:101], 0
	v_mfma_f32_16x16x32_bf16 v[78:81], v[150:153], v[114:117], 0
	ds_read_b128 v[146:149], v189 offset:32768
	ds_read_b128 v[150:153], v189 offset:36864
	s_waitcnt lgkmcnt(6)
	v_mfma_f32_16x16x32_bf16 v[82:85], v[154:157], v[98:101], 0
	v_mfma_f32_16x16x32_bf16 v[86:89], v[154:157], v[114:117], 0
	v_mfma_f32_16x16x32_bf16 v[90:93], v[158:161], v[98:101], 0
	v_mfma_f32_16x16x32_bf16 v[94:97], v[158:161], v[114:117], 0
	ds_read_b128 v[154:157], v189 offset:40960
	ds_read_b128 v[158:161], v189 offset:45056
	s_waitcnt lgkmcnt(6)
	v_mfma_f32_16x16x32_bf16 v[66:69], v[198:201], v[102:105], v[66:69]
	v_mfma_f32_16x16x32_bf16 v[70:73], v[198:201], v[118:121], v[70:73]
	v_mfma_f32_16x16x32_bf16 v[74:77], v[202:205], v[102:105], v[74:77]
	v_mfma_f32_16x16x32_bf16 v[78:81], v[202:205], v[118:121], v[78:81]
	ds_read_b128 v[198:201], v190 offset:32768
	ds_read_b128 v[202:205], v190 offset:36864
	s_waitcnt lgkmcnt(6)
; #define SBAR() __builtin_amdgcn_sched_barrier(0)
; #define RESC(a) do { if (__any((a) < 1.f)) { if (hi == 0) al_l[r32] = (a); asm volatile("s_waitcnt lgkmcnt(0)" ::: "memory"); \
;     for (int d = 0; d < 4; ++d) for (int r = 0; r < 16; ++r) o[d][r] *= al_l[crow(r, hi)]; } } while (0)
; #define RESC(a) do { if (__any((a) < 1.f)) { if (hi == 0) al_l[r32] = (a); asm volatile("s_waitcnt lgkmcnt(0)" ::: "memory"); \
;     for (int d = 0; d < 4; ++d) for (int r = 0; r < 16; ++r) o[d][r] *= al_l[crow(r, hi)]; } } while (0)
; #define ATT_SYNC(jn) do { ATT_WAIT_BAR(); if ((jn) < NT) ATT_DMA((jn), (jn) & 3); } while (0)
; __device__ __forceinline__ void attn_dma_body(const bf16_t* __restrict__ Qb, int ldq, int tpos0, const float* __restrict__ rope, const float* __restrict__ qgain, ...
;     ...
;   for (int j = 1; j + 1 < NT; j += 2) {
;     { SBAR(); qkt(pB0, pB1, (const bf16_t*)(lds + (j & 3) * SHM_SLOT), qr, r32, hi);
;       finishSM(pA0, pA1, alA, l_reg, pa0, pa1, pa2, pa3); s16x4 va[8]; pv_rd<0>(va, vb0 + ((j - 1) & 3) * (int)SHM_SLOT); SBAR();
;       if (!lead) ATT_SYNC(j + 2);
;       pv_d0_pre(o, vb0 + ((j - 1) & 3) * (int)SHM_SLOT, va, pa0, pa1, pa2, pa3); partialSM(pB0, pB1, m_reg, mnB, alB);
;       if (lead) ATT_SYNC(j + 2);
;       RESC(alB); }
;     { SBAR(); qkt(pA0, pA1, (const bf16_t*)(lds + ((j + 1) & 3) * SHM_SLOT), qr, r32, hi);
;       finishSM(pB0, pB1, alB, l_reg, pa0, pa1, pa2, pa3); s16x4 va[8]; pv_rd<0>(va, vb0 + (j & 3) * (int)SHM_SLOT); SBAR();
;       if (!lead) ATT_SYNC(j + 3);
;       pv_d0_pre(o, vb0 + (j & 3) * (int)SHM_SLOT, va, pa0, pa1, pa2, pa3); partialSM(pA0, pA1, m_reg, mnA, alA);
;       if (lead) ATT_SYNC(j + 3);
;       RESC(alA); }
;   }
	v_mfma_f32_16x16x32_bf16 v[82:85], v[206:209], v[102:105], v[82:85]
	v_mfma_f32_16x16x32_bf16 v[86:89], v[206:209], v[118:121], v[86:89]
	v_mfma_f32_16x16x32_bf16 v[90:93], v[210:213], v[102:105], v[90:93]
	v_mfma_f32_16x16x32_bf16 v[94:97], v[210:213], v[118:121], v[94:97]
	ds_read_b128 v[206:209], v190 offset:40960
	ds_read_b128 v[210:213], v190 offset:45056
	s_waitcnt lgkmcnt(6)
	v_mfma_f32_16x16x32_bf16 v[66:69], v[146:149], v[106:109], v[66:69]
	v_mfma_f32_16x16x32_bf16 v[70:73], v[146:149], v[122:125], v[70:73]
	v_mfma_f32_16x16x32_bf16 v[74:77], v[150:153], v[106:109], v[74:77]
	v_mfma_f32_16x16x32_bf16 v[78:81], v[150:153], v[122:125], v[78:81]
	s_waitcnt lgkmcnt(4)
	v_mfma_f32_16x16x32_bf16 v[82:85], v[154:157], v[106:109], v[82:85]
	v_mfma_f32_16x16x32_bf16 v[86:89], v[154:157], v[122:125], v[86:89]
	v_mfma_f32_16x16x32_bf16 v[90:93], v[158:161], v[106:109], v[90:93]
	v_mfma_f32_16x16x32_bf16 v[94:97], v[158:161], v[122:125], v[94:97]
	s_waitcnt lgkmcnt(2)
	v_mfma_f32_16x16x32_bf16 v[66:69], v[198:201], v[110:113], v[66:69]
	v_mfma_f32_16x16x32_bf16 v[70:73], v[198:201], v[126:129], v[70:73]
	v_mfma_f32_16x16x32_bf16 v[74:77], v[202:205], v[110:113], v[74:77]
	v_mfma_f32_16x16x32_bf16 v[78:81], v[202:205], v[126:129], v[78:81]
	ds_read_b64_tr_b16 v[214:215], v180 offset:0
	ds_read_b64_tr_b16 v[216:217], v180 offset:4096
	ds_read_b64_tr_b16 v[218:219], v181 offset:0
	ds_read_b64_tr_b16 v[220:221], v181 offset:4096
	ds_read_b64_tr_b16 v[222:223], v180 offset:512
	ds_read_b64_tr_b16 v[224:225], v180 offset:4608
	ds_read_b64_tr_b16 v[226:227], v181 offset:512
	ds_read_b64_tr_b16 v[228:229], v181 offset:4608
	ds_read_b64_tr_b16 v[230:231], v180 offset:1024
	ds_read_b64_tr_b16 v[232:233], v180 offset:5120
	ds_read_b64_tr_b16 v[234:235], v181 offset:1024
	ds_read_b64_tr_b16 v[236:237], v181 offset:5120
	s_waitcnt lgkmcnt(12)
	v_mfma_f32_16x16x32_bf16 v[82:85], v[206:209], v[110:113], v[82:85]
	v_mfma_f32_16x16x32_bf16 v[86:89], v[206:209], v[126:129], v[86:89]
	v_mfma_f32_16x16x32_bf16 v[90:93], v[210:213], v[110:113], v[90:93]
	v_mfma_f32_16x16x32_bf16 v[94:97], v[210:213], v[126:129], v[94:97]
	s_waitcnt lgkmcnt(8)
	v_mfma_f32_16x16x32_bf16 v[2:5], v[214:217], v[130:133], v[2:5]
	v_exp_f32_e32 v66, v66
	v_mfma_f32_16x16x32_bf16 v[6:9], v[214:217], v[138:141], v[6:9]
	v_exp_f32_e32 v67, v67
	v_mfma_f32_16x16x32_bf16 v[10:13], v[218:221], v[130:133], v[10:13]
	v_exp_f32_e32 v68, v68
	v_mfma_f32_16x16x32_bf16 v[14:17], v[218:221], v[138:141], v[14:17]
	v_exp_f32_e32 v69, v69
	ds_read_b64_tr_b16 v[238:239], v180 offset:1536
	ds_read_b64_tr_b16 v[240:241], v180 offset:5632
	ds_read_b64_tr_b16 v[242:243], v181 offset:1536
	ds_read_b64_tr_b16 v[244:245], v181 offset:5632
	s_waitcnt lgkmcnt(8)
	v_mfma_f32_16x16x32_bf16 v[18:21], v[222:225], v[130:133], v[18:21]
	v_exp_f32_e32 v70, v70
	v_mfma_f32_16x16x32_bf16 v[22:25], v[222:225], v[138:141], v[22:25]
	v_exp_f32_e32 v71, v71
	v_mfma_f32_16x16x32_bf16 v[26:29], v[226:229], v[130:133], v[26:29]
	v_exp_f32_e32 v72, v72
	v_mfma_f32_16x16x32_bf16 v[30:33], v[226:229], v[138:141], v[30:33]
	v_exp_f32_e32 v73, v73
	v_mfma_f32_16x16x32_bf16 v[246:249], v[194:197], v[130:133], v[246:249]
	ds_read_b64_tr_b16 v[214:215], v180 offset:8192
	ds_read_b64_tr_b16 v[216:217], v180 offset:12288
	ds_read_b64_tr_b16 v[218:219], v181 offset:8192
	ds_read_b64_tr_b16 v[220:221], v181 offset:12288
	s_waitcnt lgkmcnt(8)
	v_mfma_f32_16x16x32_bf16 v[34:37], v[230:233], v[130:133], v[34:37]
	v_exp_f32_e32 v74, v74
	v_mfma_f32_16x16x32_bf16 v[38:41], v[230:233], v[138:141], v[38:41]
	v_exp_f32_e32 v75, v75
	v_mfma_f32_16x16x32_bf16 v[42:45], v[234:237], v[130:133], v[42:45]
	v_exp_f32_e32 v76, v76
	v_mfma_f32_16x16x32_bf16 v[46:49], v[234:237], v[138:141], v[46:49]
	v_exp_f32_e32 v77, v77
	ds_read_b64_tr_b16 v[222:223], v180 offset:8704
	ds_read_b64_tr_b16 v[224:225], v180 offset:12800
	ds_read_b64_tr_b16 v[226:227], v181 offset:8704
	ds_read_b64_tr_b16 v[228:229], v181 offset:12800
	s_waitcnt lgkmcnt(8)
	v_mfma_f32_16x16x32_bf16 v[50:53], v[238:241], v[130:133], v[50:53]
	v_exp_f32_e32 v78, v78
	v_mfma_f32_16x16x32_bf16 v[54:57], v[238:241], v[138:141], v[54:57]
	v_exp_f32_e32 v79, v79
	v_mfma_f32_16x16x32_bf16 v[58:61], v[242:245], v[130:133], v[58:61]
	v_exp_f32_e32 v80, v80
	v_mfma_f32_16x16x32_bf16 v[62:65], v[242:245], v[138:141], v[62:65]
	v_exp_f32_e32 v81, v81
	v_mfma_f32_16x16x32_bf16 v[252:255], v[194:197], v[138:141], v[252:255]
	ds_read_b64_tr_b16 v[230:231], v180 offset:9216
	ds_read_b64_tr_b16 v[232:233], v180 offset:13312
	ds_read_b64_tr_b16 v[234:235], v181 offset:9216
	ds_read_b64_tr_b16 v[236:237], v181 offset:13312
	s_waitcnt lgkmcnt(8)
	v_mfma_f32_16x16x32_bf16 v[2:5], v[214:217], v[134:137], v[2:5]
	v_exp_f32_e32 v82, v82
	v_mfma_f32_16x16x32_bf16 v[6:9], v[214:217], v[142:145], v[6:9]
	v_exp_f32_e32 v83, v83
	v_mfma_f32_16x16x32_bf16 v[10:13], v[218:221], v[134:137], v[10:13]
	v_exp_f32_e32 v84, v84
	v_mfma_f32_16x16x32_bf16 v[14:17], v[218:221], v[142:145], v[14:17]
	v_exp_f32_e32 v85, v85
	ds_read_b64_tr_b16 v[238:239], v180 offset:9728
	ds_read_b64_tr_b16 v[240:241], v180 offset:13824
	ds_read_b64_tr_b16 v[242:243], v181 offset:9728
	ds_read_b64_tr_b16 v[244:245], v181 offset:13824
	s_waitcnt lgkmcnt(8)
	v_mfma_f32_16x16x32_bf16 v[18:21], v[222:225], v[134:137], v[18:21]
	v_exp_f32_e32 v86, v86
	v_mfma_f32_16x16x32_bf16 v[22:25], v[222:225], v[142:145], v[22:25]
	v_exp_f32_e32 v87, v87
	v_mfma_f32_16x16x32_bf16 v[26:29], v[226:229], v[134:137], v[26:29]
	v_exp_f32_e32 v88, v88
	v_mfma_f32_16x16x32_bf16 v[30:33], v[226:229], v[142:145], v[30:33]
	v_exp_f32_e32 v89, v89
	v_mfma_f32_16x16x32_bf16 v[246:249], v[194:197], v[134:137], v[246:249]
	s_waitcnt lgkmcnt(4)
	v_mfma_f32_16x16x32_bf16 v[34:37], v[230:233], v[134:137], v[34:37]
	v_exp_f32_e32 v90, v90
	v_mfma_f32_16x16x32_bf16 v[38:41], v[230:233], v[142:145], v[38:41]
	v_exp_f32_e32 v91, v91
	v_mfma_f32_16x16x32_bf16 v[42:45], v[234:237], v[134:137], v[42:45]
	v_exp_f32_e32 v92, v92
	v_mfma_f32_16x16x32_bf16 v[46:49], v[234:237], v[142:145], v[46:49]
	v_exp_f32_e32 v93, v93
	s_waitcnt lgkmcnt(0)
	v_mfma_f32_16x16x32_bf16 v[50:53], v[238:241], v[134:137], v[50:53]
	v_exp_f32_e32 v94, v94
	v_mfma_f32_16x16x32_bf16 v[54:57], v[238:241], v[142:145], v[54:57]
	v_exp_f32_e32 v95, v95
	v_mfma_f32_16x16x32_bf16 v[58:61], v[242:245], v[134:137], v[58:61]
	v_exp_f32_e32 v96, v96
	v_mfma_f32_16x16x32_bf16 v[62:65], v[242:245], v[142:145], v[62:65]
	v_exp_f32_e32 v97, v97
	v_mfma_f32_16x16x32_bf16 v[252:255], v[194:197], v[142:145], v[252:255]
	s_waitcnt vmcnt(0) lgkmcnt(0)
	s_barrier
	s_cmp_ge_u32 s97, 130
	s_cbranch_scc1 .Lf16_se_L2
	s_add_i32 m0, s96, 0x8000
	s_nop 0
	global_load_lds_dwordx4 v170, s[2:3]
	s_add_i32 m0, s96, 0xa000
	s_nop 0
	global_load_lds_dwordx4 v172, s[2:3]
	s_add_i32 m0, s96, 0xc000
	s_nop 0
	global_load_lds_dwordx4 v171, s[2:3]
	s_add_i32 m0, s96, 0xe000
	s_nop 0
	global_load_lds_dwordx4 v173, s[2:3]
	s_add_u32 s2, s2, 0x4000
	s_addc_u32 s3, s3, 0
; #define SBAR() __builtin_amdgcn_sched_barrier(0)
; #define RESC(a) do { if (__any((a) < 1.f)) { if (hi == 0) al_l[r32] = (a); asm volatile("s_waitcnt lgkmcnt(0)" ::: "memory"); \
;     for (int d = 0; d < 4; ++d) for (int r = 0; r < 16; ++r) o[d][r] *= al_l[crow(r, hi)]; } } while (0)
; #define RESC(a) do { if (__any((a) < 1.f)) { if (hi == 0) al_l[r32] = (a); asm volatile("s_waitcnt lgkmcnt(0)" ::: "memory"); \
;     for (int d = 0; d < 4; ++d) for (int r = 0; r < 16; ++r) o[d][r] *= al_l[crow(r, hi)]; } } while (0)
; #define ATT_SYNC(jn) do { ATT_WAIT_BAR(); if ((jn) < NT) ATT_DMA((jn), (jn) & 3); } while (0)
; __device__ __forceinline__ void attn_dma_body(const bf16_t* __restrict__ Qb, int ldq, int tpos0, const float* __restrict__ rope, const float* __restrict__ qgain, ...
;     ...
;   for (int j = 1; j + 1 < NT; j += 2) {
;     { SBAR(); qkt(pB0, pB1, (const bf16_t*)(lds + (j & 3) * SHM_SLOT), qr, r32, hi);
;       finishSM(pA0, pA1, alA, l_reg, pa0, pa1, pa2, pa3); s16x4 va[8]; pv_rd<0>(va, vb0 + ((j - 1) & 3) * (int)SHM_SLOT); SBAR();
;       if (!lead) ATT_SYNC(j + 2);
;       pv_d0_pre(o, vb0 + ((j - 1) & 3) * (int)SHM_SLOT, va, pa0, pa1, pa2, pa3); partialSM(pB0, pB1, m_reg, mnB, alB);
;       if (lead) ATT_SYNC(j + 2);
;       RESC(alB); }
;     { SBAR(); qkt(pA0, pA1, (const bf16_t*)(lds + ((j + 1) & 3) * SHM_SLOT), qr, r32, hi);
;       finishSM(pB0, pB1, alB, l_reg, pa0, pa1, pa2, pa3); s16x4 va[8]; pv_rd<0>(va, vb0 + (j & 3) * (int)SHM_SLOT); SBAR();
;       if (!lead) ATT_SYNC(j + 3);
;       pv_d0_pre(o, vb0 + (j & 3) * (int)SHM_SLOT, va, pa0, pa1, pa2, pa3); partialSM(pA0, pA1, m_reg, mnA, alA);
;       if (lead) ATT_SYNC(j + 3);
;       RESC(alA); }
;   }
.Lf16_se_L2:
	v_cvt_pk_bf16_f32 v130, v66, v67
	v_cvt_pk_bf16_f32 v131, v68, v69
	v_cvt_pk_bf16_f32 v132, v74, v75
	v_cvt_pk_bf16_f32 v133, v76, v77
	v_cvt_pk_bf16_f32 v134, v82, v83
	v_cvt_pk_bf16_f32 v135, v84, v85
	v_cvt_pk_bf16_f32 v136, v90, v91
	v_cvt_pk_bf16_f32 v137, v92, v93
	v_cvt_pk_bf16_f32 v138, v70, v71
	v_cvt_pk_bf16_f32 v139, v72, v73
	v_cvt_pk_bf16_f32 v140, v78, v79
	v_cvt_pk_bf16_f32 v141, v80, v81
	v_cvt_pk_bf16_f32 v142, v86, v87
	v_cvt_pk_bf16_f32 v143, v88, v89
	v_cvt_pk_bf16_f32 v144, v94, v95
	v_cvt_pk_bf16_f32 v145, v96, v97
	s_add_i32 s97, s97, 1
	s_cmp_lt_u32 s97, 132
	s_cbranch_scc0 .Lf16_done
	ds_read_b128 v[146:149], v183 offset:0
	ds_read_b128 v[150:153], v183 offset:4096
	ds_read_b128 v[154:157], v183 offset:8192
	ds_read_b128 v[158:161], v183 offset:12288
	ds_read_b128 v[198:201], v184 offset:0
	ds_read_b128 v[202:205], v184 offset:4096
	ds_read_b128 v[206:209], v184 offset:8192
	ds_read_b128 v[210:213], v184 offset:12288
	s_waitcnt lgkmcnt(6)
	v_mfma_f32_16x16x32_bf16 v[66:69], v[146:149], v[98:101], 0
	v_mfma_f32_16x16x32_bf16 v[70:73], v[146:149], v[114:117], 0
	v_mfma_f32_16x16x32_bf16 v[74:77], v[150:153], v[98:101], 0
	v_mfma_f32_16x16x32_bf16 v[78:81], v[150:153], v[114:117], 0
	ds_read_b128 v[146:149], v185 offset:0
	ds_read_b128 v[150:153], v185 offset:4096
	s_waitcnt lgkmcnt(6)
	v_mfma_f32_16x16x32_bf16 v[82:85], v[154:157], v[98:101], 0
	v_mfma_f32_16x16x32_bf16 v[86:89], v[154:157], v[114:117], 0
	v_mfma_f32_16x16x32_bf16 v[90:93], v[158:161], v[98:101], 0
	v_mfma_f32_16x16x32_bf16 v[94:97], v[158:161], v[114:117], 0
	ds_read_b128 v[154:157], v185 offset:8192
	ds_read_b128 v[158:161], v185 offset:12288
	s_waitcnt lgkmcnt(6)
	v_mfma_f32_16x16x32_bf16 v[66:69], v[198:201], v[102:105], v[66:69]
	v_mfma_f32_16x16x32_bf16 v[70:73], v[198:201], v[118:121], v[70:73]
	v_mfma_f32_16x16x32_bf16 v[74:77], v[202:205], v[102:105], v[74:77]
	v_mfma_f32_16x16x32_bf16 v[78:81], v[202:205], v[118:121], v[78:81]
	ds_read_b128 v[198:201], v186 offset:0
	ds_read_b128 v[202:205], v186 offset:4096
	s_waitcnt lgkmcnt(6)
	v_mfma_f32_16x16x32_bf16 v[82:85], v[206:209], v[102:105], v[82:85]
	v_mfma_f32_16x16x32_bf16 v[86:89], v[206:209], v[118:121], v[86:89]
	v_mfma_f32_16x16x32_bf16 v[90:93], v[210:213], v[102:105], v[90:93]
	v_mfma_f32_16x16x32_bf16 v[94:97], v[210:213], v[118:121], v[94:97]
	ds_read_b128 v[206:209], v186 offset:8192
	ds_read_b128 v[210:213], v186 offset:12288
	s_waitcnt lgkmcnt(6)
	v_mfma_f32_16x16x32_bf16 v[66:69], v[146:149], v[106:109], v[66:69]
	v_mfma_f32_16x16x32_bf16 v[70:73], v[146:149], v[122:125], v[70:73]
	v_mfma_f32_16x16x32_bf16 v[74:77], v[150:153], v[106:109], v[74:77]
	v_mfma_f32_16x16x32_bf16 v[78:81], v[150:153], v[122:125], v[78:81]
	s_waitcnt lgkmcnt(4)
	v_mfma_f32_16x16x32_bf16 v[82:85], v[154:157], v[106:109], v[82:85]
	v_mfma_f32_16x16x32_bf16 v[86:89], v[154:157], v[122:125], v[86:89]
	v_mfma_f32_16x16x32_bf16 v[90:93], v[158:161], v[106:109], v[90:93]
	v_mfma_f32_16x16x32_bf16 v[94:97], v[158:161], v[122:125], v[94:97]
	s_waitcnt lgkmcnt(2)
	v_mfma_f32_16x16x32_bf16 v[66:69], v[198:201], v[110:113], v[66:69]
	v_mfma_f32_16x16x32_bf16 v[70:73], v[198:201], v[126:129], v[70:73]
	v_mfma_f32_16x16x32_bf16 v[74:77], v[202:205], v[110:113], v[74:77]
	v_mfma_f32_16x16x32_bf16 v[78:81], v[202:205], v[126:129], v[78:81]
	ds_read_b64_tr_b16 v[214:215], v180 offset:32768
	ds_read_b64_tr_b16 v[216:217], v180 offset:36864
	ds_read_b64_tr_b16 v[218:219], v181 offset:32768
	ds_read_b64_tr_b16 v[220:221], v181 offset:36864
	ds_read_b64_tr_b16 v[222:223], v180 offset:33280
	ds_read_b64_tr_b16 v[224:225], v180 offset:37376
	ds_read_b64_tr_b16 v[226:227], v181 offset:33280
	ds_read_b64_tr_b16 v[228:229], v181 offset:37376
	ds_read_b64_tr_b16 v[230:231], v180 offset:33792
	ds_read_b64_tr_b16 v[232:233], v180 offset:37888
	ds_read_b64_tr_b16 v[234:235], v181 offset:33792
	ds_read_b64_tr_b16 v[236:237], v181 offset:37888
	s_waitcnt lgkmcnt(12)
	v_mfma_f32_16x16x32_bf16 v[82:85], v[206:209], v[110:113], v[82:85]
	v_mfma_f32_16x16x32_bf16 v[86:89], v[206:209], v[126:129], v[86:89]
	v_mfma_f32_16x16x32_bf16 v[90:93], v[210:213], v[110:113], v[90:93]
	v_mfma_f32_16x16x32_bf16 v[94:97], v[210:213], v[126:129], v[94:97]
	s_waitcnt lgkmcnt(8)
	v_mfma_f32_16x16x32_bf16 v[2:5], v[214:217], v[130:133], v[2:5]
	v_exp_f32_e32 v66, v66
	v_mfma_f32_16x16x32_bf16 v[6:9], v[214:217], v[138:141], v[6:9]
	v_exp_f32_e32 v67, v67
	v_mfma_f32_16x16x32_bf16 v[10:13], v[218:221], v[130:133], v[10:13]
	v_exp_f32_e32 v68, v68
	v_mfma_f32_16x16x32_bf16 v[14:17], v[218:221], v[138:141], v[14:17]
	v_exp_f32_e32 v69, v69
	ds_read_b64_tr_b16 v[238:239], v180 offset:34304
	ds_read_b64_tr_b16 v[240:241], v180 offset:38400
	ds_read_b64_tr_b16 v[242:243], v181 offset:34304
	ds_read_b64_tr_b16 v[244:245], v181 offset:38400
	s_waitcnt lgkmcnt(8)
	v_mfma_f32_16x16x32_bf16 v[18:21], v[222:225], v[130:133], v[18:21]
	v_exp_f32_e32 v70, v70
	v_mfma_f32_16x16x32_bf16 v[22:25], v[222:225], v[138:141], v[22:25]
	v_exp_f32_e32 v71, v71
	v_mfma_f32_16x16x32_bf16 v[26:29], v[226:229], v[130:133], v[26:29]
	v_exp_f32_e32 v72, v72
	v_mfma_f32_16x16x32_bf16 v[30:33], v[226:229], v[138:141], v[30:33]
	v_exp_f32_e32 v73, v73
	v_mfma_f32_16x16x32_bf16 v[246:249], v[194:197], v[130:133], v[246:249]
	ds_read_b64_tr_b16 v[214:215], v180 offset:40960
	ds_read_b64_tr_b16 v[216:217], v180 offset:45056
	ds_read_b64_tr_b16 v[218:219], v181 offset:40960
	ds_read_b64_tr_b16 v[220:221], v181 offset:45056
	s_waitcnt lgkmcnt(8)
; #define SBAR() __builtin_amdgcn_sched_barrier(0)
; #define RESC(a) do { if (__any((a) < 1.f)) { if (hi == 0) al_l[r32] = (a); asm volatile("s_waitcnt lgkmcnt(0)" ::: "memory"); \
;     for (int d = 0; d < 4; ++d) for (int r = 0; r < 16; ++r) o[d][r] *= al_l[crow(r, hi)]; } } while (0)
; #define RESC(a) do { if (__any((a) < 1.f)) { if (hi == 0) al_l[r32] = (a); asm volatile("s_waitcnt lgkmcnt(0)" ::: "memory"); \
;     for (int d = 0; d < 4; ++d) for (int r = 0; r < 16; ++r) o[d][r] *= al_l[crow(r, hi)]; } } while (0)
; #define ATT_SYNC(jn) do { ATT_WAIT_BAR(); if ((jn) < NT) ATT_DMA((jn), (jn) & 3); } while (0)
; __device__ __forceinline__ void attn_dma_body(const bf16_t* __restrict__ Qb, int ldq, int tpos0, const float* __restrict__ rope, const float* __restrict__ qgain, ...
;     ...
;   for (int j = 1; j + 1 < NT; j += 2) {
;     { SBAR(); qkt(pB0, pB1, (const bf16_t*)(lds + (j & 3) * SHM_SLOT), qr, r32, hi);
;       finishSM(pA0, pA1, alA, l_reg, pa0, pa1, pa2, pa3); s16x4 va[8]; pv_rd<0>(va, vb0 + ((j - 1) & 3) * (int)SHM_SLOT); SBAR();
;       if (!lead) ATT_SYNC(j + 2);
;       pv_d0_pre(o, vb0 + ((j - 1) & 3) * (int)SHM_SLOT, va, pa0, pa1, pa2, pa3); partialSM(pB0, pB1, m_reg, mnB, alB);
;       if (lead) ATT_SYNC(j + 2);
;       RESC(alB); }
;     { SBAR(); qkt(pA0, pA1, (const bf16_t*)(lds + ((j + 1) & 3) * SHM_SLOT), qr, r32, hi);
;       finishSM(pB0, pB1, alB, l_reg, pa0, pa1, pa2, pa3); s16x4 va[8]; pv_rd<0>(va, vb0 + (j & 3) * (int)SHM_SLOT); SBAR();
;       if (!lead) ATT_SYNC(j + 3);
;       pv_d0_pre(o, vb0 + (j & 3) * (int)SHM_SLOT, va, pa0, pa1, pa2, pa3); partialSM(pA0, pA1, m_reg, mnA, alA);
;       if (lead) ATT_SYNC(j + 3);
;       RESC(alA); }
;   }
;     ...
;   { SBAR(); qkt(pB0, pB1, (const bf16_t*)(lds + ((NT - 1) & 3) * SHM_SLOT), qr, r32, hi);
;     finishSM(pA0, pA1, alA, l_reg, pa0, pa1, pa2, pa3); SBAR();
;     pv_d0(o, vb0 + ((NT - 2) & 3) * (int)SHM_SLOT, pa0, pa1, pa2, pa3); partialSM(pB0, pB1, m_reg, mnB, alB);
;     RESC(alB);
;     finishSM(pB0, pB1, alB, l_reg, pa0, pa1, pa2, pa3); SBAR();
;     pv_d0(o, vb0 + ((NT - 1) & 3) * (int)SHM_SLOT, pa0, pa1, pa2, pa3); }
	v_mfma_f32_16x16x32_bf16 v[34:37], v[230:233], v[130:133], v[34:37]
	v_exp_f32_e32 v74, v74
	v_mfma_f32_16x16x32_bf16 v[38:41], v[230:233], v[138:141], v[38:41]
	v_exp_f32_e32 v75, v75
	v_mfma_f32_16x16x32_bf16 v[42:45], v[234:237], v[130:133], v[42:45]
	v_exp_f32_e32 v76, v76
	v_mfma_f32_16x16x32_bf16 v[46:49], v[234:237], v[138:141], v[46:49]
	v_exp_f32_e32 v77, v77
	ds_read_b64_tr_b16 v[222:223], v180 offset:41472
	ds_read_b64_tr_b16 v[224:225], v180 offset:45568
	ds_read_b64_tr_b16 v[226:227], v181 offset:41472
	ds_read_b64_tr_b16 v[228:229], v181 offset:45568
	s_waitcnt lgkmcnt(8)
	v_mfma_f32_16x16x32_bf16 v[50:53], v[238:241], v[130:133], v[50:53]
	v_exp_f32_e32 v78, v78
	v_mfma_f32_16x16x32_bf16 v[54:57], v[238:241], v[138:141], v[54:57]
	v_exp_f32_e32 v79, v79
	v_mfma_f32_16x16x32_bf16 v[58:61], v[242:245], v[130:133], v[58:61]
	v_exp_f32_e32 v80, v80
	v_mfma_f32_16x16x32_bf16 v[62:65], v[242:245], v[138:141], v[62:65]
	v_exp_f32_e32 v81, v81
	v_mfma_f32_16x16x32_bf16 v[252:255], v[194:197], v[138:141], v[252:255]
	ds_read_b64_tr_b16 v[230:231], v180 offset:41984
	ds_read_b64_tr_b16 v[232:233], v180 offset:46080
	ds_read_b64_tr_b16 v[234:235], v181 offset:41984
	ds_read_b64_tr_b16 v[236:237], v181 offset:46080
	s_waitcnt lgkmcnt(8)
	v_mfma_f32_16x16x32_bf16 v[2:5], v[214:217], v[134:137], v[2:5]
	v_exp_f32_e32 v82, v82
	v_mfma_f32_16x16x32_bf16 v[6:9], v[214:217], v[142:145], v[6:9]
	v_exp_f32_e32 v83, v83
	v_mfma_f32_16x16x32_bf16 v[10:13], v[218:221], v[134:137], v[10:13]
	v_exp_f32_e32 v84, v84
	v_mfma_f32_16x16x32_bf16 v[14:17], v[218:221], v[142:145], v[14:17]
	v_exp_f32_e32 v85, v85
	ds_read_b64_tr_b16 v[238:239], v180 offset:42496
	ds_read_b64_tr_b16 v[240:241], v180 offset:46592
	ds_read_b64_tr_b16 v[242:243], v181 offset:42496
	ds_read_b64_tr_b16 v[244:245], v181 offset:46592
	s_waitcnt lgkmcnt(8)
	v_mfma_f32_16x16x32_bf16 v[18:21], v[222:225], v[134:137], v[18:21]
	v_exp_f32_e32 v86, v86
	v_mfma_f32_16x16x32_bf16 v[22:25], v[222:225], v[142:145], v[22:25]
	v_exp_f32_e32 v87, v87
	v_mfma_f32_16x16x32_bf16 v[26:29], v[226:229], v[134:137], v[26:29]
	v_exp_f32_e32 v88, v88
	v_mfma_f32_16x16x32_bf16 v[30:33], v[226:229], v[142:145], v[30:33]
	v_exp_f32_e32 v89, v89
	v_mfma_f32_16x16x32_bf16 v[246:249], v[194:197], v[134:137], v[246:249]
	s_waitcnt lgkmcnt(4)
	v_mfma_f32_16x16x32_bf16 v[34:37], v[230:233], v[134:137], v[34:37]
	v_exp_f32_e32 v90, v90
	v_mfma_f32_16x16x32_bf16 v[38:41], v[230:233], v[142:145], v[38:41]
	v_exp_f32_e32 v91, v91
	v_mfma_f32_16x16x32_bf16 v[42:45], v[234:237], v[134:137], v[42:45]
	v_exp_f32_e32 v92, v92
	v_mfma_f32_16x16x32_bf16 v[46:49], v[234:237], v[142:145], v[46:49]
	v_exp_f32_e32 v93, v93
	s_waitcnt lgkmcnt(0)
	v_mfma_f32_16x16x32_bf16 v[50:53], v[238:241], v[134:137], v[50:53]
	v_exp_f32_e32 v94, v94
	v_mfma_f32_16x16x32_bf16 v[54:57], v[238:241], v[142:145], v[54:57]
	v_exp_f32_e32 v95, v95
	v_mfma_f32_16x16x32_bf16 v[58:61], v[242:245], v[134:137], v[58:61]
	v_exp_f32_e32 v96, v96
	v_mfma_f32_16x16x32_bf16 v[62:65], v[242:245], v[142:145], v[62:65]
	v_exp_f32_e32 v97, v97
	v_mfma_f32_16x16x32_bf16 v[252:255], v[194:197], v[142:145], v[252:255]
	s_waitcnt vmcnt(0) lgkmcnt(0)
	s_barrier
	s_cmp_ge_u32 s97, 130
	s_cbranch_scc1 .Lf16_se_L3
	s_add_i32 m0, s96, 0x10000
	s_nop 0
	global_load_lds_dwordx4 v170, s[2:3]
	s_add_i32 m0, s96, 0x12000
	s_nop 0
	global_load_lds_dwordx4 v172, s[2:3]
	s_add_i32 m0, s96, 0x14000
	s_nop 0
	global_load_lds_dwordx4 v171, s[2:3]
	s_add_i32 m0, s96, 0x16000
	s_nop 0
	global_load_lds_dwordx4 v173, s[2:3]
	s_add_u32 s2, s2, 0x4000
	s_addc_u32 s3, s3, 0
.Lf16_se_L3:
	v_cvt_pk_bf16_f32 v130, v66, v67
	v_cvt_pk_bf16_f32 v131, v68, v69
	v_cvt_pk_bf16_f32 v132, v74, v75
	v_cvt_pk_bf16_f32 v133, v76, v77
	v_cvt_pk_bf16_f32 v134, v82, v83
	v_cvt_pk_bf16_f32 v135, v84, v85
	v_cvt_pk_bf16_f32 v136, v90, v91
	v_cvt_pk_bf16_f32 v137, v92, v93
	v_cvt_pk_bf16_f32 v138, v70, v71
	v_cvt_pk_bf16_f32 v139, v72, v73
	v_cvt_pk_bf16_f32 v140, v78, v79
	v_cvt_pk_bf16_f32 v141, v80, v81
	v_cvt_pk_bf16_f32 v142, v86, v87
	v_cvt_pk_bf16_f32 v143, v88, v89
	v_cvt_pk_bf16_f32 v144, v94, v95
	v_cvt_pk_bf16_f32 v145, v96, v97
	s_add_i32 s97, s97, 1
	s_branch .Lf16_L_loop
.Lf16_done:
	s_mov_b32 s37, 0x18000
	ds_read_b64_tr_b16 v[214:215], v180 offset:32768
	ds_read_b64_tr_b16 v[216:217], v180 offset:36864
	ds_read_b64_tr_b16 v[218:219], v181 offset:32768
	ds_read_b64_tr_b16 v[220:221], v181 offset:36864
	ds_read_b64_tr_b16 v[222:223], v180 offset:33280
	ds_read_b64_tr_b16 v[224:225], v180 offset:37376
	ds_read_b64_tr_b16 v[226:227], v181 offset:33280
	ds_read_b64_tr_b16 v[228:229], v181 offset:37376
	ds_read_b64_tr_b16 v[230:231], v180 offset:33792
	ds_read_b64_tr_b16 v[232:233], v180 offset:37888
	ds_read_b64_tr_b16 v[234:235], v181 offset:33792
	ds_read_b64_tr_b16 v[236:237], v181 offset:37888
	s_waitcnt lgkmcnt(8)
	v_mfma_f32_16x16x32_bf16 v[2:5], v[214:217], v[130:133], v[2:5]
	v_mfma_f32_16x16x32_bf16 v[6:9], v[214:217], v[138:141], v[6:9]
	v_mfma_f32_16x16x32_bf16 v[10:13], v[218:221], v[130:133], v[10:13]
	v_mfma_f32_16x16x32_bf16 v[14:17], v[218:221], v[138:141], v[14:17]
	ds_read_b64_tr_b16 v[238:239], v180 offset:34304
	ds_read_b64_tr_b16 v[240:241], v180 offset:38400
	ds_read_b64_tr_b16 v[242:243], v181 offset:34304
	ds_read_b64_tr_b16 v[244:245], v181 offset:38400
	s_waitcnt lgkmcnt(8)
	v_mfma_f32_16x16x32_bf16 v[18:21], v[222:225], v[130:133], v[18:21]
	v_mfma_f32_16x16x32_bf16 v[22:25], v[222:225], v[138:141], v[22:25]
	v_mfma_f32_16x16x32_bf16 v[26:29], v[226:229], v[130:133], v[26:29]
	v_mfma_f32_16x16x32_bf16 v[30:33], v[226:229], v[138:141], v[30:33]
	v_mfma_f32_16x16x32_bf16 v[246:249], v[194:197], v[130:133], v[246:249]
	ds_read_b64_tr_b16 v[214:215], v180 offset:40960
	ds_read_b64_tr_b16 v[216:217], v180 offset:45056
	ds_read_b64_tr_b16 v[218:219], v181 offset:40960
	ds_read_b64_tr_b16 v[220:221], v181 offset:45056
	s_waitcnt lgkmcnt(8)
; #define SBAR() __builtin_amdgcn_sched_barrier(0)
; __device__ __forceinline__ int crow(int r, int hi) { return (r & 3) + 8 * (r >> 2) + 4 * hi; }
; #define RESC(a) do { if (__any((a) < 1.f)) { if (hi == 0) al_l[r32] = (a); asm volatile("s_waitcnt lgkmcnt(0)" ::: "memory"); \
;     for (int d = 0; d < 4; ++d) for (int r = 0; r < 16; ++r) o[d][r] *= al_l[crow(r, hi)]; } } while (0)
; #define RESC(a) do { if (__any((a) < 1.f)) { if (hi == 0) al_l[r32] = (a); asm volatile("s_waitcnt lgkmcnt(0)" ::: "memory"); \
;     for (int d = 0; d < 4; ++d) for (int r = 0; r < 16; ++r) o[d][r] *= al_l[crow(r, hi)]; } } while (0)
; __device__ __forceinline__ void attn_dma_body(const bf16_t* __restrict__ Qb, int ldq, int tpos0, const float* __restrict__ rope, const float* __restrict__ qgain, ...
;     ...
;   { SBAR(); qkt(pB0, pB1, (const bf16_t*)(lds + ((NT - 1) & 3) * SHM_SLOT), qr, r32, hi);
;     finishSM(pA0, pA1, alA, l_reg, pa0, pa1, pa2, pa3); SBAR();
;     pv_d0(o, vb0 + ((NT - 2) & 3) * (int)SHM_SLOT, pa0, pa1, pa2, pa3); partialSM(pB0, pB1, m_reg, mnB, alB);
;     RESC(alB);
;     finishSM(pB0, pB1, alB, l_reg, pa0, pa1, pa2, pa3); SBAR();
;     pv_d0(o, vb0 + ((NT - 1) & 3) * (int)SHM_SLOT, pa0, pa1, pa2, pa3); }
;   if (hi == 0) li_l[r32] = l_reg; asm volatile("s_waitcnt lgkmcnt(0)" ::: "memory");
;   float rli[16];
; #pragma unroll
;   for (int r = 0; r < 16; ++r) rli[r] = __builtin_amdgcn_rcpf(li_l[crow(r, hi)]);
	v_mfma_f32_16x16x32_bf16 v[34:37], v[230:233], v[130:133], v[34:37]
	v_mfma_f32_16x16x32_bf16 v[38:41], v[230:233], v[138:141], v[38:41]
	v_mfma_f32_16x16x32_bf16 v[42:45], v[234:237], v[130:133], v[42:45]
	v_mfma_f32_16x16x32_bf16 v[46:49], v[234:237], v[138:141], v[46:49]
	ds_read_b64_tr_b16 v[222:223], v180 offset:41472
	ds_read_b64_tr_b16 v[224:225], v180 offset:45568
	ds_read_b64_tr_b16 v[226:227], v181 offset:41472
	ds_read_b64_tr_b16 v[228:229], v181 offset:45568
	s_waitcnt lgkmcnt(8)
	v_mfma_f32_16x16x32_bf16 v[50:53], v[238:241], v[130:133], v[50:53]
	v_mfma_f32_16x16x32_bf16 v[54:57], v[238:241], v[138:141], v[54:57]
	v_mfma_f32_16x16x32_bf16 v[58:61], v[242:245], v[130:133], v[58:61]
	v_mfma_f32_16x16x32_bf16 v[62:65], v[242:245], v[138:141], v[62:65]
	v_mfma_f32_16x16x32_bf16 v[252:255], v[194:197], v[138:141], v[252:255]
	ds_read_b64_tr_b16 v[230:231], v180 offset:41984
	ds_read_b64_tr_b16 v[232:233], v180 offset:46080
	ds_read_b64_tr_b16 v[234:235], v181 offset:41984
	ds_read_b64_tr_b16 v[236:237], v181 offset:46080
	s_waitcnt lgkmcnt(8)
	v_mfma_f32_16x16x32_bf16 v[2:5], v[214:217], v[134:137], v[2:5]
	v_mfma_f32_16x16x32_bf16 v[6:9], v[214:217], v[142:145], v[6:9]
	v_mfma_f32_16x16x32_bf16 v[10:13], v[218:221], v[134:137], v[10:13]
	v_mfma_f32_16x16x32_bf16 v[14:17], v[218:221], v[142:145], v[14:17]
	ds_read_b64_tr_b16 v[238:239], v180 offset:42496
	ds_read_b64_tr_b16 v[240:241], v180 offset:46592
	ds_read_b64_tr_b16 v[242:243], v181 offset:42496
	ds_read_b64_tr_b16 v[244:245], v181 offset:46592
	s_waitcnt lgkmcnt(8)
	v_mfma_f32_16x16x32_bf16 v[18:21], v[222:225], v[134:137], v[18:21]
	v_mfma_f32_16x16x32_bf16 v[22:25], v[222:225], v[142:145], v[22:25]
	v_mfma_f32_16x16x32_bf16 v[26:29], v[226:229], v[134:137], v[26:29]
	v_mfma_f32_16x16x32_bf16 v[30:33], v[226:229], v[142:145], v[30:33]
	v_mfma_f32_16x16x32_bf16 v[246:249], v[194:197], v[134:137], v[246:249]
	s_waitcnt lgkmcnt(4)
	v_mfma_f32_16x16x32_bf16 v[34:37], v[230:233], v[134:137], v[34:37]
	v_mfma_f32_16x16x32_bf16 v[38:41], v[230:233], v[142:145], v[38:41]
	v_mfma_f32_16x16x32_bf16 v[42:45], v[234:237], v[134:137], v[42:45]
	v_mfma_f32_16x16x32_bf16 v[46:49], v[234:237], v[142:145], v[46:49]
	s_waitcnt lgkmcnt(0)
	v_mfma_f32_16x16x32_bf16 v[50:53], v[238:241], v[134:137], v[50:53]
	v_mfma_f32_16x16x32_bf16 v[54:57], v[238:241], v[142:145], v[54:57]
	v_mfma_f32_16x16x32_bf16 v[58:61], v[242:245], v[134:137], v[58:61]
	v_mfma_f32_16x16x32_bf16 v[62:65], v[242:245], v[142:145], v[62:65]
	v_mfma_f32_16x16x32_bf16 v[252:255], v[194:197], v[142:145], v[252:255]
	s_nop 7
	s_nop 7
	v_mov_b32_e32 v182, v246
	v_mov_b32_e32 v195, v252
	v_rcp_f32_e32 v182, v182
	v_rcp_f32_e32 v195, v195
	s_waitcnt lgkmcnt(0)
	s_barrier
; __device__ __forceinline__ unsigned f2bf(float f) { unsigned u = __builtin_bit_cast(unsigned, f); return (u + 0x7fffu + ((u >> 16) & 1u)) >> 16; }
; __device__ __forceinline__ int crow(int r, int hi) { return (r & 3) + 8 * (r >> 2) + 4 * hi; }
; #define ATT_WAIT_BAR() asm volatile("s_waitcnt vmcnt(0) lgkmcnt(0)\n\ts_barrier" ::: "memory")
; __device__ __forceinline__ void attn_dma_body(const bf16_t* __restrict__ Qb, int ldq, int tpos0, const float* __restrict__ rope, const float* __restrict__ qgain, ...
;     ...
;   if (hi == 0) li_l[r32] = l_reg; asm volatile("s_waitcnt lgkmcnt(0)" ::: "memory");
;   float rli[16];
; #pragma unroll
;   for (int r = 0; r < 16; ++r) rli[r] = __builtin_amdgcn_rcpf(li_l[crow(r, hi)]);
;   bf16_t* Ow = Ob + (long)(wid * QBLK) * LDO;
;   asm volatile("s_waitcnt lgkmcnt(0)\n\ts_barrier" ::: "memory");
;   { char* st = lds + wid * 8704;
; #pragma unroll
;     for (int r = 0; r < 16; ++r) { const int orow = crow(r, hi);
; #pragma unroll
;       for (int d0 = 0; d0 < 4; ++d0) *(bf16_t*)(st + orow * 272 + (d0 * 32 + r32) * 2) = (bf16_t)f2bf(o[d0][r] * rli[r]); }
;     asm volatile("s_waitcnt lgkmcnt(0)" ::: "memory");
; #pragma unroll
;     for (int i = 0; i < 8; ++i) { const int c = i * 64 + lane, row = c >> 4, cc = c & 15; const u32x4 v = *(const u32x4*)(st + row * 272 + cc * 16);
;       const bf16_t* gp = Ow + (long)row * LDO + cc * 8;
;       asm volatile("global_store_dwordx4 %0, %1, off sc1\n\ts_nop 1" :: "v"(gp), "v"(v) : "memory"); } }
;   ATT_WAIT_BAR();
	v_mul_u32_u24_e32 v84, 0x2200, v179
	v_and_b32_e32 v246, 15, v167
	v_lshrrev_b32_e32 v247, 4, v167
	v_mul_u32_u24_e32 v248, 0x110, v246
	v_add_u32_e32 v248, v248, v84
	v_lshl_add_u32 v248, v247, 3, v248
	v_mul_f32_e32 v2, v2, v182
	v_mul_f32_e32 v3, v3, v182
	v_mul_f32_e32 v4, v4, v182
	v_mul_f32_e32 v5, v5, v182
	v_cvt_pk_bf16_f32 v252, v2, v3
	v_cvt_pk_bf16_f32 v253, v4, v5
	ds_write_b64 v248, v[252:253] offset:0
	v_mul_f32_e32 v6, v6, v195
	v_mul_f32_e32 v7, v7, v195
	v_mul_f32_e32 v8, v8, v195
	v_mul_f32_e32 v9, v9, v195
	v_cvt_pk_bf16_f32 v254, v6, v7
	v_cvt_pk_bf16_f32 v255, v8, v9
	ds_write_b64 v248, v[254:255] offset:4352
	v_mul_f32_e32 v10, v10, v182
	v_mul_f32_e32 v11, v11, v182
	v_mul_f32_e32 v12, v12, v182
	v_mul_f32_e32 v13, v13, v182
	v_cvt_pk_bf16_f32 v252, v10, v11
	v_cvt_pk_bf16_f32 v253, v12, v13
	ds_write_b64 v248, v[252:253] offset:32
	v_mul_f32_e32 v14, v14, v195
	v_mul_f32_e32 v15, v15, v195
	v_mul_f32_e32 v16, v16, v195
	v_mul_f32_e32 v17, v17, v195
	v_cvt_pk_bf16_f32 v254, v14, v15
	v_cvt_pk_bf16_f32 v255, v16, v17
	ds_write_b64 v248, v[254:255] offset:4384
	v_mul_f32_e32 v18, v18, v182
	v_mul_f32_e32 v19, v19, v182
	v_mul_f32_e32 v20, v20, v182
	v_mul_f32_e32 v21, v21, v182
	v_cvt_pk_bf16_f32 v252, v18, v19
	v_cvt_pk_bf16_f32 v253, v20, v21
	ds_write_b64 v248, v[252:253] offset:64
	v_mul_f32_e32 v22, v22, v195
	v_mul_f32_e32 v23, v23, v195
	v_mul_f32_e32 v24, v24, v195
	v_mul_f32_e32 v25, v25, v195
	v_cvt_pk_bf16_f32 v254, v22, v23
	v_cvt_pk_bf16_f32 v255, v24, v25
	ds_write_b64 v248, v[254:255] offset:4416
	v_mul_f32_e32 v26, v26, v182
	v_mul_f32_e32 v27, v27, v182
	v_mul_f32_e32 v28, v28, v182
	v_mul_f32_e32 v29, v29, v182
	v_cvt_pk_bf16_f32 v252, v26, v27
	v_cvt_pk_bf16_f32 v253, v28, v29
	ds_write_b64 v248, v[252:253] offset:96
	v_mul_f32_e32 v30, v30, v195
	v_mul_f32_e32 v31, v31, v195
	v_mul_f32_e32 v32, v32, v195
	v_mul_f32_e32 v33, v33, v195
	v_cvt_pk_bf16_f32 v254, v30, v31
	v_cvt_pk_bf16_f32 v255, v32, v33
	ds_write_b64 v248, v[254:255] offset:4448
	v_mul_f32_e32 v34, v34, v182
	v_mul_f32_e32 v35, v35, v182
	v_mul_f32_e32 v36, v36, v182
	v_mul_f32_e32 v37, v37, v182
	v_cvt_pk_bf16_f32 v252, v34, v35
	v_cvt_pk_bf16_f32 v253, v36, v37
	ds_write_b64 v248, v[252:253] offset:128
	v_mul_f32_e32 v38, v38, v195
	v_mul_f32_e32 v39, v39, v195
	v_mul_f32_e32 v40, v40, v195
	v_mul_f32_e32 v41, v41, v195
	v_cvt_pk_bf16_f32 v254, v38, v39
	v_cvt_pk_bf16_f32 v255, v40, v41
	ds_write_b64 v248, v[254:255] offset:4480
	v_mul_f32_e32 v42, v42, v182
	v_mul_f32_e32 v43, v43, v182
	v_mul_f32_e32 v44, v44, v182
	v_mul_f32_e32 v45, v45, v182
	v_cvt_pk_bf16_f32 v252, v42, v43
	v_cvt_pk_bf16_f32 v253, v44, v45
	ds_write_b64 v248, v[252:253] offset:160
	v_mul_f32_e32 v46, v46, v195
	v_mul_f32_e32 v47, v47, v195
	v_mul_f32_e32 v48, v48, v195
	v_mul_f32_e32 v49, v49, v195
	v_cvt_pk_bf16_f32 v254, v46, v47
	v_cvt_pk_bf16_f32 v255, v48, v49
	ds_write_b64 v248, v[254:255] offset:4512
	v_mul_f32_e32 v50, v50, v182
	v_mul_f32_e32 v51, v51, v182
	v_mul_f32_e32 v52, v52, v182
	v_mul_f32_e32 v53, v53, v182
	v_cvt_pk_bf16_f32 v252, v50, v51
	v_cvt_pk_bf16_f32 v253, v52, v53
	ds_write_b64 v248, v[252:253] offset:192
	v_mul_f32_e32 v54, v54, v195
	v_mul_f32_e32 v55, v55, v195
	v_mul_f32_e32 v56, v56, v195
	v_mul_f32_e32 v57, v57, v195
	v_cvt_pk_bf16_f32 v254, v54, v55
	v_cvt_pk_bf16_f32 v255, v56, v57
	ds_write_b64 v248, v[254:255] offset:4544
	v_mul_f32_e32 v58, v58, v182
	v_mul_f32_e32 v59, v59, v182
	v_mul_f32_e32 v60, v60, v182
	v_mul_f32_e32 v61, v61, v182
	v_cvt_pk_bf16_f32 v252, v58, v59
	v_cvt_pk_bf16_f32 v253, v60, v61
	ds_write_b64 v248, v[252:253] offset:224
	v_mul_f32_e32 v62, v62, v195
	v_mul_f32_e32 v63, v63, v195
	v_mul_f32_e32 v64, v64, v195
	v_mul_f32_e32 v65, v65, v195
	v_cvt_pk_bf16_f32 v254, v62, v63
	v_cvt_pk_bf16_f32 v255, v64, v65
	ds_write_b64 v248, v[254:255] offset:4576
	s_waitcnt lgkmcnt(0)
	s_lshl_b64 s[6:7], s[70:71], 12
	s_add_u32 s6, s23, s6
	s_addc_u32 s7, s94, s7
	s_add_u32 s6, s6, s44
	s_addc_u32 s7, s7, s45
	v_ashrrev_i32_e32 v165, 31, v164
	v_lshlrev_b64 v[66:67], 12, v[164:165]
	v_lshl_add_u64 v[6:7], s[6:7], 0, v[66:67]
	v_lshlrev_b32_e32 v162, 4, v246
	v_lshl_add_u64 v[6:7], v[6:7], 0, v[162:163]
	v_lshlrev_b32_e32 v162, 12, v247
	v_lshl_add_u64 v[6:7], v[6:7], 0, v[162:163]
	v_mul_u32_u24_e32 v249, 0x110, v247
	v_add_u32_e32 v249, v249, v84
	v_lshl_add_u32 v249, v246, 4, v249
	ds_read_b128 v[10:13], v249 offset:0
	s_mov_b64 s[8:9], 0x0
	v_lshl_add_u64 v[8:9], v[6:7], 0, s[8:9]
	s_waitcnt lgkmcnt(0)
	global_store_dwordx4 v[8:9], v[10:13], off sc1
	s_nop 1
	ds_read_b128 v[14:17], v249 offset:1088
	s_mov_b64 s[8:9], 0x4000
	v_lshl_add_u64 v[8:9], v[6:7], 0, s[8:9]
	s_waitcnt lgkmcnt(0)
	global_store_dwordx4 v[8:9], v[14:17], off sc1
	s_nop 1
	ds_read_b128 v[10:13], v249 offset:2176
	s_mov_b64 s[8:9], 0x8000
	v_lshl_add_u64 v[8:9], v[6:7], 0, s[8:9]
	s_waitcnt lgkmcnt(0)
	global_store_dwordx4 v[8:9], v[10:13], off sc1
	s_nop 1
	ds_read_b128 v[14:17], v249 offset:3264
	s_mov_b64 s[8:9], 0xc000
	v_lshl_add_u64 v[8:9], v[6:7], 0, s[8:9]
	s_waitcnt lgkmcnt(0)
	global_store_dwordx4 v[8:9], v[14:17], off sc1
	s_nop 1
	ds_read_b128 v[10:13], v249 offset:4352
	s_mov_b64 s[8:9], 0x10000
	v_lshl_add_u64 v[8:9], v[6:7], 0, s[8:9]
	s_waitcnt lgkmcnt(0)
	global_store_dwordx4 v[8:9], v[10:13], off sc1
	s_nop 1
	ds_read_b128 v[14:17], v249 offset:5440
	s_mov_b64 s[8:9], 0x14000
	v_lshl_add_u64 v[8:9], v[6:7], 0, s[8:9]
	s_waitcnt lgkmcnt(0)
	global_store_dwordx4 v[8:9], v[14:17], off sc1
	s_nop 1
	ds_read_b128 v[10:13], v249 offset:6528
	s_mov_b64 s[8:9], 0x18000
	v_lshl_add_u64 v[8:9], v[6:7], 0, s[8:9]
	s_waitcnt lgkmcnt(0)
	global_store_dwordx4 v[8:9], v[10:13], off sc1
	s_nop 1
	ds_read_b128 v[14:17], v249 offset:7616
	s_mov_b64 s[8:9], 0x1c000
	v_lshl_add_u64 v[8:9], v[6:7], 0, s[8:9]
	s_waitcnt lgkmcnt(0)
	global_store_dwordx4 v[8:9], v[14:17], off sc1
	s_nop 1
	s_waitcnt vmcnt(0) lgkmcnt(0)
	s_barrier
	v_readlane_b32 s96, v250, 4
	v_readlane_b32 s97, v250, 5
	s_setprio 0
	s_branch .LBB0_437
